# v43 + one s_nop in two load segments per K-loop so that every MFMA run sits at the same 8-byte phase (4), loop heads pinned at offset 36 mod 64
# baseline (speedup 1.0000x reference)
; #define PG8_STAGE(bufoff, gbase, voff) do { _Pragma("unroll") for (int _i = 0; _i < 2; ++_i) \
;         __builtin_amdgcn_global_load_lds((const unsigned*)((const char*)(gbase) + (voff)[_i]), (PG8_LAS unsigned*)(lds + (bufoff) + ldsw + _i * 8192), 16, 0, 0); } while (0)
; #define PG8_LDA(dst, b, h) do { _Pragma("unroll") for (int m = 0; m < 4; ++m) _Pragma("unroll") for (int k = 0; k < 2; ++k) dst[m][k] = *(const PG8_LAS bf16x8*)(lds + PG8_SA(b, h) + aoff + m * 2048 + k * 1024); } while (0)
; #define PG8_LDB(dst, b, h) do { _Pragma("unroll") for (int n = 0; n < 2; ++n) _Pragma("unroll") for (int k = 0; k < 2; ++k) dst[n][k] = *(const PG8_LAS bf16x8*)(lds + PG8_SB(b, h) + boff + n * 2048 + k * 1024); } while (0)
; #define PG8_MMA(ai, bj, At, Bt) do { __builtin_amdgcn_s_setprio(1); _Pragma("unroll") for (int m = 0; m < 4; ++m) _Pragma("unroll") for (int n = 0; n < 2; ++n) _Pragma("unroll") for (int k = 0; k < 2; ++k) \
;         acc[ai][bj][m][n] = __builtin_amdgcn_mfma_f32_16x16x32_bf16(Bt[n][k], At[m][k], acc[ai][bj][m][n], 0, 0, 0); __builtin_amdgcn_s_setprio(0); } while (0)
; #define PG8_WAIT_V(n) asm volatile("s_waitcnt vmcnt(" #n ")" ::: "memory")
; #define PG8_WAIT_L(n) asm volatile("s_waitcnt lgkmcnt(" #n ")" ::: "memory")
; #define PG8_BAR __builtin_amdgcn_s_barrier()
; #define PG8_SCHED __builtin_amdgcn_sched_barrier(0)
; template <class Epi, class Sched, bool ALIGN_EPI = false, bool SP2 = false>
; __device__ __forceinline__ void gemm_phase(PG8_LAS unsigned char* lds, const Gemm g, const Sched& S, const Epi& E) {
;     ...
;             PG8_LDB(B0, 0, 0); PG8_LDB(B1, 0, 1); PG8_SCHED; PG8_LDA(At, 0, 0); PG8_STAGE(PG8_SA(1, 1), a1 + hstep, voffA);
;     ...
;             if (PROBE_KIND == 18 && t == 0 && ui > 0 && g.probe) { const unsigned long long tq_ = __builtin_amdgcn_s_memrealtime(); PG8_WAIT_V(8); pg8_probe_acc += (unsigned)(__builtin_amdgcn_s_memrealtime() - tq_); }
;     ...
;             PG8_WAIT_V(8); PG8_WAIT_L(0); PG8_BAR; PG8_MMA(0, 0, At, B0); PG8_MMA(0, 1, At, B1); PG8_BAR; PG8_SCHED;
;             PG8_LDA(At, 0, 1); PG8_STAGE(PG8_SB(0, 0), b2, voffB); PG8_STAGE(PG8_SB(0, 1), b2 + hstep, voffB); PG8_STAGE(PG8_SA(0, 0), a2, voffA);
;             PG8_WAIT_V(8); PG8_WAIT_L(0); PG8_BAR; if (cur.half == 0) { PG8_MMA(1, 0, At, B0); PG8_MMA(1, 1, At, B1); } PG8_BAR; PG8_SCHED;
.Lpj_ip_1:
	s_waitcnt lgkmcnt(0)
	s_barrier
	s_setprio 1
	s_waitcnt lgkmcnt(0)
	v_mfma_f32_16x16x32_bf16 v[128:131], v[132:135], v[182:185], 0
	v_mfma_f32_16x16x32_bf16 v[124:127], v[140:143], v[182:185], 0
	v_mfma_f32_16x16x32_bf16 v[112:115], v[132:135], v[190:193], 0
	v_mfma_f32_16x16x32_bf16 v[108:111], v[140:143], v[190:193], 0
	v_mfma_f32_16x16x32_bf16 v[96:99], v[132:135], v[198:201], 0
	v_mfma_f32_16x16x32_bf16 v[92:95], v[140:143], v[198:201], 0
	v_mfma_f32_16x16x32_bf16 v[80:83], v[132:135], v[212:215], 0
	v_mfma_f32_16x16x32_bf16 v[76:79], v[140:143], v[212:215], 0
	v_mfma_f32_16x16x32_bf16 v[128:131], v[136:139], v[186:189], v[128:131]
	v_mfma_f32_16x16x32_bf16 v[124:127], v[144:147], v[186:189], v[124:127]
	v_mfma_f32_16x16x32_bf16 v[112:115], v[136:139], v[194:197], v[112:115]
	v_mfma_f32_16x16x32_bf16 v[108:111], v[144:147], v[194:197], v[108:111]
	v_mfma_f32_16x16x32_bf16 v[96:99], v[136:139], v[208:211], v[96:99]
	v_mfma_f32_16x16x32_bf16 v[92:95], v[144:147], v[208:211], v[92:95]
	v_mfma_f32_16x16x32_bf16 v[80:83], v[136:139], v[216:219], v[80:83]
	v_mfma_f32_16x16x32_bf16 v[76:79], v[144:147], v[216:219], v[76:79]
	s_setprio 0
	s_setprio 1
	v_mfma_f32_16x16x32_bf16 v[120:123], v[148:151], v[182:185], 0
	v_mfma_f32_16x16x32_bf16 v[116:119], v[156:159], v[182:185], 0
	v_mfma_f32_16x16x32_bf16 v[104:107], v[148:151], v[190:193], 0
	v_mfma_f32_16x16x32_bf16 v[100:103], v[156:159], v[190:193], 0
	v_mfma_f32_16x16x32_bf16 v[88:91], v[148:151], v[198:201], 0
	v_mfma_f32_16x16x32_bf16 v[84:87], v[156:159], v[198:201], 0
	v_mfma_f32_16x16x32_bf16 v[72:75], v[148:151], v[212:215], 0
	v_mfma_f32_16x16x32_bf16 v[68:71], v[156:159], v[212:215], 0
	v_mfma_f32_16x16x32_bf16 v[120:123], v[152:155], v[186:189], v[120:123]
	v_mfma_f32_16x16x32_bf16 v[116:119], v[160:163], v[186:189], v[116:119]
	v_mfma_f32_16x16x32_bf16 v[104:107], v[152:155], v[194:197], v[104:107]
	v_mfma_f32_16x16x32_bf16 v[100:103], v[160:163], v[194:197], v[100:103]
	v_mfma_f32_16x16x32_bf16 v[88:91], v[152:155], v[208:211], v[88:91]
	v_mfma_f32_16x16x32_bf16 v[84:87], v[160:163], v[208:211], v[84:87]
	v_mfma_f32_16x16x32_bf16 v[72:75], v[152:155], v[216:219], v[72:75]
	v_mfma_f32_16x16x32_bf16 v[68:71], v[160:163], v[216:219], v[68:71]
	s_setprio 0
	s_barrier
	s_add_i32 s61, s61, s27
	v_lshl_add_u64 v[228:229], s[0:1], 0, v[166:167]
	s_mov_b32 m0, s61
	ds_read_b128 v[182:185], v206 offset:16384
	ds_read_b128 v[186:189], v206 offset:17408
	ds_read_b128 v[190:193], v206 offset:18432
	ds_read_b128 v[194:197], v206 offset:19456
	ds_read_b128 v[198:201], v206 offset:20480
	ds_read_b128 v[208:211], v206 offset:21504
	ds_read_b128 v[212:215], v206 offset:22528
	ds_read_b128 v[216:219], v206 offset:23552
	global_load_lds_dwordx4 v[228:229], off
	s_add_i32 m0, s61, 0x2000
	s_add_u32 s78, s0, 0x40000
	v_lshl_add_u64 v[230:231], s[0:1], 0, v[170:171]
	s_addc_u32 s79, s1, 0
	s_add_i32 s61, s63, s27
	global_load_lds_dwordx4 v[230:231], off
	v_lshl_add_u64 v[232:233], s[78:79], 0, v[166:167]
	s_mov_b32 m0, s61
	v_lshl_add_u64 v[234:235], s[10:11], 0, v[168:169]
	global_load_lds_dwordx4 v[232:233], off
	v_lshl_add_u64 v[232:233], s[78:79], 0, v[170:171]
	s_add_i32 m0, s61, 0x2000
	s_nop 0
	global_load_lds_dwordx4 v[232:233], off
	v_lshl_add_u64 v[232:233], s[10:11], 0, v[164:165]
	s_mov_b32 m0, s19
	s_nop 0
	global_load_lds_dwordx4 v[232:233], off
	s_mov_b32 m0, s30
	s_nop 0
	global_load_lds_dwordx4 v[234:235], off
	s_cmp_eq_u32 s32, 0
	s_cbranch_scc1 .Lpw_ip_2
	s_waitcnt vmcnt(24)
	s_branch .Lpj_ip_2
	.p2align 6
	s_nop 0
	s_nop 0
	s_nop 0
	s_nop 0
	s_nop 0
	s_nop 0
	s_nop 0
	s_nop 0
	s_nop 0

;     __device__ __forceinline__ void a_ready(const Unit&) const { if (++ncall == 3 && sig != nullptr && threadIdx.x == 0) __hip_atomic_fetch_add(sig, 1u, __ATOMIC_RELAXED, __HIP_MEMORY_SCOPE_AGENT); }
; #define PG8_STAGE(bufoff, gbase, voff) do { _Pragma("unroll") for (int _i = 0; _i < 2; ++_i) \
;         __builtin_amdgcn_global_load_lds((const unsigned*)((const char*)(gbase) + (voff)[_i]), (PG8_LAS unsigned*)(lds + (bufoff) + ldsw + _i * 8192), 16, 0, 0); } while (0)
; #define PG8_LDA(dst, b, h) do { _Pragma("unroll") for (int m = 0; m < 4; ++m) _Pragma("unroll") for (int k = 0; k < 2; ++k) dst[m][k] = *(const PG8_LAS bf16x8*)(lds + PG8_SA(b, h) + aoff + m * 2048 + k * 1024); } while (0)
; #define PG8_BAR __builtin_amdgcn_s_barrier()
; template <class Epi, class Sched, bool ALIGN_EPI = false, bool SP2 = false>
; __device__ __forceinline__ void gemm_phase(PG8_LAS unsigned char* lds, const Gemm g, const Sched& S, const Epi& E) {
;     ...
;         for (int t = 0; t < nt; t += 2) {
;             const bool last = (t == nt - 2);
;             const char* a1 = cA + (size_t)(t + 1) * kstep;
;             const char* a2 = last ? nA : cA + (size_t)(t + 2) * kstep; const char* b2 = last ? nB : cB + (size_t)(t + 2) * kstep;
;             const char* a3 = a2 + kstep; const char* b3 = b2 + kstep;
;             if (last && has_next) S.a_ready(nxt);
;             if constexpr (SP2) {
;             PG8_LDB(B0, 0, 0); PG8_LDB(B1, 0, 1); PG8_SCHED; PG8_LDA(At, 0, 0); PG8_STAGE(PG8_SA(1, 1), a1 + hstep, voffA);
;     ...
;             if (PROBE_KIND == 18 && t == 0 && ui > 0 && g.probe) { const unsigned long long tq_ = __builtin_amdgcn_s_memrealtime(); PG8_WAIT_V(8); pg8_probe_acc += (unsigned)(__builtin_amdgcn_s_memrealtime() - tq_); }
;     ...
;             PG8_WAIT_V(8); PG8_WAIT_L(0); PG8_BAR; PG8_MMA(0, 0, At, B0); PG8_MMA(0, 1, At, B1); PG8_BAR; PG8_SCHED;
;             PG8_LDA(At, 0, 1); PG8_STAGE(PG8_SB(0, 0), b2, voffB); PG8_STAGE(PG8_SB(0, 1), b2 + hstep, voffB); PG8_STAGE(PG8_SA(0, 0), a2, voffA);
;             PG8_WAIT_V(8); PG8_WAIT_L(0); PG8_BAR; if (cur.half == 0) { PG8_MMA(1, 0, At, B0); PG8_MMA(1, 1, At, B1); } PG8_BAR; PG8_SCHED;
;             PG8_LDB(B0, 1, 0); PG8_LDB(B1, 1, 1); PG8_SCHED; PG8_LDA(At, 1, 0); PG8_STAGE(PG8_SA(0, 1), a2 + hstep, voffA);
;             PG8_WAIT_V(8); PG8_WAIT_L(0); PG8_BAR; PG8_MMA(0, 0, At, B0); PG8_MMA(0, 1, At, B1); PG8_BAR; PG8_SCHED;
.LBB0_395:
	s_add_u32 s0, s8, 0xfffc0080
	s_addc_u32 s1, s9, -1
	s_add_i32 s61, 0, 0x10000
	s_cmp_eq_u32 s39, 12
	s_cselect_b32 s11, s12, s1
	s_cselect_b32 s10, s13, s0
	v_add_u32_e32 v2, s61, v203
	s_cselect_b32 s1, s14, s38
	s_cselect_b32 s0, s15, s36
	s_add_i32 s63, 0, 0x14000
	ds_read_b128 v[132:135], v2
	ds_read_b128 v[136:139], v2 offset:1024
	ds_read_b128 v[140:143], v2 offset:2048
	ds_read_b128 v[144:147], v2 offset:3072
	v_add_u32_e32 v2, s63, v203
	ds_read_b128 v[148:151], v2
	ds_read_b128 v[152:155], v2 offset:1024
	ds_read_b128 v[156:159], v2 offset:2048
	ds_read_b128 v[160:163], v2 offset:3072
	v_lshl_add_u64 v[228:229], s[8:9], 0, v[178:179]
	s_add_i32 m0, s19, 0xc000
	ds_read_b128 v[182:185], v206
	ds_read_b128 v[186:189], v206 offset:1024
	ds_read_b128 v[190:193], v206 offset:2048
	ds_read_b128 v[194:197], v206 offset:3072
	ds_read_b128 v[198:201], v206 offset:4096
	ds_read_b128 v[208:211], v206 offset:5120
	ds_read_b128 v[212:215], v206 offset:6144
	ds_read_b128 v[216:219], v206 offset:7168
	global_load_lds_dwordx4 v[228:229], off
	v_lshl_add_u64 v[228:229], s[8:9], 0, v[180:181]
	s_add_i32 m0, s19, 0xe000
	s_nop 0
	global_load_lds_dwordx4 v[228:229], off
	s_waitcnt vmcnt(8)
	s_waitcnt lgkmcnt(0)
	s_barrier
	s_setprio 1
	s_waitcnt lgkmcnt(0)
	v_mfma_f32_16x16x32_bf16 v[128:131], v[132:135], v[182:185], v[128:131]
	v_mfma_f32_16x16x32_bf16 v[124:127], v[140:143], v[182:185], v[124:127]
	v_mfma_f32_16x16x32_bf16 v[112:115], v[132:135], v[190:193], v[112:115]
	v_mfma_f32_16x16x32_bf16 v[108:111], v[140:143], v[190:193], v[108:111]
	v_mfma_f32_16x16x32_bf16 v[96:99], v[132:135], v[198:201], v[96:99]
	v_mfma_f32_16x16x32_bf16 v[92:95], v[140:143], v[198:201], v[92:95]
	v_mfma_f32_16x16x32_bf16 v[80:83], v[132:135], v[212:215], v[80:83]
	v_mfma_f32_16x16x32_bf16 v[76:79], v[140:143], v[212:215], v[76:79]
	v_mfma_f32_16x16x32_bf16 v[128:131], v[136:139], v[186:189], v[128:131]
	v_mfma_f32_16x16x32_bf16 v[124:127], v[144:147], v[186:189], v[124:127]
	v_mfma_f32_16x16x32_bf16 v[112:115], v[136:139], v[194:197], v[112:115]
	v_mfma_f32_16x16x32_bf16 v[108:111], v[144:147], v[194:197], v[108:111]
	v_mfma_f32_16x16x32_bf16 v[96:99], v[136:139], v[208:211], v[96:99]
	v_mfma_f32_16x16x32_bf16 v[92:95], v[144:147], v[208:211], v[92:95]
	v_mfma_f32_16x16x32_bf16 v[80:83], v[136:139], v[216:219], v[80:83]
	v_mfma_f32_16x16x32_bf16 v[76:79], v[144:147], v[216:219], v[76:79]
	s_setprio 0
	s_setprio 1
	v_mfma_f32_16x16x32_bf16 v[120:123], v[148:151], v[182:185], v[120:123]
	v_mfma_f32_16x16x32_bf16 v[116:119], v[156:159], v[182:185], v[116:119]
	v_mfma_f32_16x16x32_bf16 v[104:107], v[148:151], v[190:193], v[104:107]
	v_mfma_f32_16x16x32_bf16 v[100:103], v[156:159], v[190:193], v[100:103]
	v_mfma_f32_16x16x32_bf16 v[88:91], v[148:151], v[198:201], v[88:91]
	v_mfma_f32_16x16x32_bf16 v[84:87], v[156:159], v[198:201], v[84:87]
	v_mfma_f32_16x16x32_bf16 v[72:75], v[148:151], v[212:215], v[72:75]
	v_mfma_f32_16x16x32_bf16 v[68:71], v[156:159], v[212:215], v[68:71]
	v_mfma_f32_16x16x32_bf16 v[120:123], v[152:155], v[186:189], v[120:123]
	v_mfma_f32_16x16x32_bf16 v[116:119], v[160:163], v[186:189], v[116:119]
	v_mfma_f32_16x16x32_bf16 v[104:107], v[152:155], v[194:197], v[104:107]
	v_mfma_f32_16x16x32_bf16 v[100:103], v[160:163], v[194:197], v[100:103]
	v_mfma_f32_16x16x32_bf16 v[88:91], v[152:155], v[208:211], v[88:91]
	v_mfma_f32_16x16x32_bf16 v[84:87], v[160:163], v[208:211], v[84:87]
	v_mfma_f32_16x16x32_bf16 v[72:75], v[152:155], v[216:219], v[72:75]
	v_mfma_f32_16x16x32_bf16 v[68:71], v[160:163], v[216:219], v[68:71]
	s_setprio 0
	s_barrier
	s_add_i32 s61, s61, s27
	v_lshl_add_u64 v[228:229], s[0:1], 0, v[166:167]
	s_mov_b32 m0, s61
	ds_read_b128 v[182:185], v206 offset:16384
	ds_read_b128 v[186:189], v206 offset:17408
	ds_read_b128 v[190:193], v206 offset:18432
	ds_read_b128 v[194:197], v206 offset:19456
	ds_read_b128 v[198:201], v206 offset:20480
	ds_read_b128 v[208:211], v206 offset:21504
	ds_read_b128 v[212:215], v206 offset:22528
	ds_read_b128 v[216:219], v206 offset:23552
	global_load_lds_dwordx4 v[228:229], off
	s_add_i32 m0, s61, 0x2000
	s_add_u32 s78, s0, 0x40000
	v_lshl_add_u64 v[230:231], s[0:1], 0, v[170:171]
	s_addc_u32 s79, s1, 0
	s_add_i32 s61, s63, s27
	global_load_lds_dwordx4 v[230:231], off
	v_lshl_add_u64 v[232:233], s[78:79], 0, v[166:167]
	s_mov_b32 m0, s61
	v_lshl_add_u64 v[234:235], s[10:11], 0, v[168:169]
	global_load_lds_dwordx4 v[232:233], off
	v_lshl_add_u64 v[232:233], s[78:79], 0, v[170:171]
	s_add_i32 m0, s61, 0x2000
	s_nop 0
	global_load_lds_dwordx4 v[232:233], off
	v_lshl_add_u64 v[232:233], s[10:11], 0, v[164:165]
	s_mov_b32 m0, s19
	s_nop 0
	global_load_lds_dwordx4 v[232:233], off
	s_mov_b32 m0, s30
	s_nop 0
	global_load_lds_dwordx4 v[234:235], off
	s_nop 0
	s_waitcnt vmcnt(8)
	s_waitcnt lgkmcnt(0)
	s_barrier
; #define PG8_STAGE(bufoff, gbase, voff) do { _Pragma("unroll") for (int _i = 0; _i < 2; ++_i) \
;         __builtin_amdgcn_global_load_lds((const unsigned*)((const char*)(gbase) + (voff)[_i]), (PG8_LAS unsigned*)(lds + (bufoff) + ldsw + _i * 8192), 16, 0, 0); } while (0)
; #define PG8_LDA(dst, b, h) do { _Pragma("unroll") for (int m = 0; m < 4; ++m) _Pragma("unroll") for (int k = 0; k < 2; ++k) dst[m][k] = *(const PG8_LAS bf16x8*)(lds + PG8_SA(b, h) + aoff + m * 2048 + k * 1024); } while (0)
; #define PG8_LDB(dst, b, h) do { _Pragma("unroll") for (int n = 0; n < 2; ++n) _Pragma("unroll") for (int k = 0; k < 2; ++k) dst[n][k] = *(const PG8_LAS bf16x8*)(lds + PG8_SB(b, h) + boff + n * 2048 + k * 1024); } while (0)
; #define PG8_MMA(ai, bj, At, Bt) do { __builtin_amdgcn_s_setprio(1); _Pragma("unroll") for (int m = 0; m < 4; ++m) _Pragma("unroll") for (int n = 0; n < 2; ++n) _Pragma("unroll") for (int k = 0; k < 2; ++k) \
;         acc[ai][bj][m][n] = __builtin_amdgcn_mfma_f32_16x16x32_bf16(Bt[n][k], At[m][k], acc[ai][bj][m][n], 0, 0, 0); __builtin_amdgcn_s_setprio(0); } while (0)
; #define PG8_WAIT_V(n) asm volatile("s_waitcnt vmcnt(" #n ")" ::: "memory")
; #define PG8_WAIT_L(n) asm volatile("s_waitcnt lgkmcnt(" #n ")" ::: "memory")
; #define PG8_BAR __builtin_amdgcn_s_barrier()
; #define PG8_SCHED __builtin_amdgcn_sched_barrier(0)
; template <class Epi, class Sched, bool ALIGN_EPI = false, bool SP2 = false>
; __device__ __forceinline__ void gemm_phase(PG8_LAS unsigned char* lds, const Gemm g, const Sched& S, const Epi& E) {
;     ...
;             PG8_WAIT_V(8); PG8_WAIT_L(0); PG8_BAR; if (cur.half == 0) { PG8_MMA(1, 0, At, B0); PG8_MMA(1, 1, At, B1); } PG8_BAR; PG8_SCHED;
;             PG8_LDB(B0, 1, 0); PG8_LDB(B1, 1, 1); PG8_SCHED; PG8_LDA(At, 1, 0); PG8_STAGE(PG8_SA(0, 1), a2 + hstep, voffA);
;             PG8_WAIT_V(8); PG8_WAIT_L(0); PG8_BAR; PG8_MMA(0, 0, At, B0); PG8_MMA(0, 1, At, B1); PG8_BAR; PG8_SCHED;
;             PG8_LDA(At, 1, 1); PG8_STAGE(PG8_SB(1, 0), b3, voffB); PG8_STAGE(PG8_SB(1, 1), b3 + hstep, voffB); PG8_STAGE(PG8_SA(1, 0), a3, voffA);
;             PG8_WAIT_V(8); PG8_WAIT_L(0); PG8_BAR; if (cur.half == 0) { PG8_MMA(1, 0, At, B0); PG8_MMA(1, 1, At, B1); } PG8_BAR; PG8_SCHED;
	s_setprio 1
	s_waitcnt lgkmcnt(0)
	v_mfma_f32_16x16x32_bf16 v[64:67], v[132:135], v[182:185], v[64:67]
	v_mfma_f32_16x16x32_bf16 v[60:63], v[140:143], v[182:185], v[60:63]
	v_mfma_f32_16x16x32_bf16 v[48:51], v[132:135], v[190:193], v[48:51]
	v_mfma_f32_16x16x32_bf16 v[44:47], v[140:143], v[190:193], v[44:47]
	v_mfma_f32_16x16x32_bf16 v[32:35], v[132:135], v[198:201], v[32:35]
	v_mfma_f32_16x16x32_bf16 v[28:31], v[140:143], v[198:201], v[28:31]
	v_mfma_f32_16x16x32_bf16 v[16:19], v[132:135], v[212:215], v[16:19]
	v_mfma_f32_16x16x32_bf16 v[12:15], v[140:143], v[212:215], v[12:15]
	v_mfma_f32_16x16x32_bf16 v[64:67], v[136:139], v[186:189], v[64:67]
	v_mfma_f32_16x16x32_bf16 v[60:63], v[144:147], v[186:189], v[60:63]
	v_mfma_f32_16x16x32_bf16 v[48:51], v[136:139], v[194:197], v[48:51]
	v_mfma_f32_16x16x32_bf16 v[44:47], v[144:147], v[194:197], v[44:47]
	v_mfma_f32_16x16x32_bf16 v[32:35], v[136:139], v[208:211], v[32:35]
	v_mfma_f32_16x16x32_bf16 v[28:31], v[144:147], v[208:211], v[28:31]
	v_mfma_f32_16x16x32_bf16 v[16:19], v[136:139], v[216:219], v[16:19]
	v_mfma_f32_16x16x32_bf16 v[12:15], v[144:147], v[216:219], v[12:15]
	s_setprio 0
	s_setprio 1
	v_mfma_f32_16x16x32_bf16 v[56:59], v[148:151], v[182:185], v[56:59]
	v_mfma_f32_16x16x32_bf16 v[52:55], v[156:159], v[182:185], v[52:55]
	v_mfma_f32_16x16x32_bf16 v[40:43], v[148:151], v[190:193], v[40:43]
	v_mfma_f32_16x16x32_bf16 v[36:39], v[156:159], v[190:193], v[36:39]
	v_mfma_f32_16x16x32_bf16 v[24:27], v[148:151], v[198:201], v[24:27]
	v_mfma_f32_16x16x32_bf16 v[20:23], v[156:159], v[198:201], v[20:23]
	v_mfma_f32_16x16x32_bf16 v[8:11], v[148:151], v[212:215], v[8:11]
	v_mfma_f32_16x16x32_bf16 v[4:7], v[156:159], v[212:215], v[4:7]
	v_mfma_f32_16x16x32_bf16 v[56:59], v[152:155], v[186:189], v[56:59]
	v_mfma_f32_16x16x32_bf16 v[52:55], v[160:163], v[186:189], v[52:55]
	v_mfma_f32_16x16x32_bf16 v[40:43], v[152:155], v[194:197], v[40:43]
	v_mfma_f32_16x16x32_bf16 v[36:39], v[160:163], v[194:197], v[36:39]
	v_mfma_f32_16x16x32_bf16 v[24:27], v[152:155], v[208:211], v[24:27]
	v_mfma_f32_16x16x32_bf16 v[20:23], v[160:163], v[208:211], v[20:23]
	v_mfma_f32_16x16x32_bf16 v[8:11], v[152:155], v[216:219], v[8:11]
	v_mfma_f32_16x16x32_bf16 v[4:7], v[160:163], v[216:219], v[4:7]
	s_setprio 0
	s_barrier
	s_add_i32 s61, 0, 0x18000
	v_add_u32_e32 v2, s61, v203
	s_add_i32 s63, 0, 0x1c000
	ds_read_b128 v[132:135], v2
	ds_read_b128 v[136:139], v2 offset:1024
	ds_read_b128 v[140:143], v2 offset:2048
	ds_read_b128 v[144:147], v2 offset:3072
	v_add_u32_e32 v2, s63, v203
	ds_read_b128 v[148:151], v2
	ds_read_b128 v[152:155], v2 offset:1024
	ds_read_b128 v[156:159], v2 offset:2048
	ds_read_b128 v[160:163], v2 offset:3072
	s_add_u32 s10, s10, 0x40000
	s_addc_u32 s11, s11, 0
	s_mov_b32 m0, s31
	v_lshl_add_u64 v[236:237], s[10:11], 0, v[164:165]
	ds_read_b128 v[182:185], v206 offset:32768
	ds_read_b128 v[186:189], v206 offset:33792
	ds_read_b128 v[190:193], v206 offset:34816
	ds_read_b128 v[194:197], v206 offset:35840
	ds_read_b128 v[198:201], v206 offset:36864
	ds_read_b128 v[208:211], v206 offset:37888
	ds_read_b128 v[212:215], v206 offset:38912
	ds_read_b128 v[216:219], v206 offset:39936
	global_load_lds_dwordx4 v[236:237], off
	v_lshl_add_u64 v[236:237], s[10:11], 0, v[168:169]
	s_mov_b32 m0, s34
	s_nop 0
	global_load_lds_dwordx4 v[236:237], off
	s_nop 0
	s_waitcnt vmcnt(8)
	s_waitcnt lgkmcnt(0)
	s_barrier
	s_setprio 1
	s_waitcnt lgkmcnt(0)
	v_mfma_f32_16x16x32_bf16 v[128:131], v[132:135], v[182:185], v[128:131]
	v_mfma_f32_16x16x32_bf16 v[124:127], v[140:143], v[182:185], v[124:127]
	v_mfma_f32_16x16x32_bf16 v[112:115], v[132:135], v[190:193], v[112:115]
	v_mfma_f32_16x16x32_bf16 v[108:111], v[140:143], v[190:193], v[108:111]
	v_mfma_f32_16x16x32_bf16 v[96:99], v[132:135], v[198:201], v[96:99]
	v_mfma_f32_16x16x32_bf16 v[92:95], v[140:143], v[198:201], v[92:95]
	v_mfma_f32_16x16x32_bf16 v[80:83], v[132:135], v[212:215], v[80:83]
	v_mfma_f32_16x16x32_bf16 v[76:79], v[140:143], v[212:215], v[76:79]
	v_mfma_f32_16x16x32_bf16 v[128:131], v[136:139], v[186:189], v[128:131]
	v_mfma_f32_16x16x32_bf16 v[124:127], v[144:147], v[186:189], v[124:127]
	v_mfma_f32_16x16x32_bf16 v[112:115], v[136:139], v[194:197], v[112:115]
	v_mfma_f32_16x16x32_bf16 v[108:111], v[144:147], v[194:197], v[108:111]
	v_mfma_f32_16x16x32_bf16 v[96:99], v[136:139], v[208:211], v[96:99]
	v_mfma_f32_16x16x32_bf16 v[92:95], v[144:147], v[208:211], v[92:95]
	v_mfma_f32_16x16x32_bf16 v[80:83], v[136:139], v[216:219], v[80:83]
	v_mfma_f32_16x16x32_bf16 v[76:79], v[144:147], v[216:219], v[76:79]
	s_setprio 0
	s_setprio 1
	v_mfma_f32_16x16x32_bf16 v[120:123], v[148:151], v[182:185], v[120:123]
	v_mfma_f32_16x16x32_bf16 v[116:119], v[156:159], v[182:185], v[116:119]
	v_mfma_f32_16x16x32_bf16 v[104:107], v[148:151], v[190:193], v[104:107]
	v_mfma_f32_16x16x32_bf16 v[100:103], v[156:159], v[190:193], v[100:103]
	v_mfma_f32_16x16x32_bf16 v[88:91], v[148:151], v[198:201], v[88:91]
	v_mfma_f32_16x16x32_bf16 v[84:87], v[156:159], v[198:201], v[84:87]
	v_mfma_f32_16x16x32_bf16 v[72:75], v[148:151], v[212:215], v[72:75]
	v_mfma_f32_16x16x32_bf16 v[68:71], v[156:159], v[212:215], v[68:71]
	v_mfma_f32_16x16x32_bf16 v[120:123], v[152:155], v[186:189], v[120:123]
	v_mfma_f32_16x16x32_bf16 v[116:119], v[160:163], v[186:189], v[116:119]
	v_mfma_f32_16x16x32_bf16 v[104:107], v[152:155], v[194:197], v[104:107]
	v_mfma_f32_16x16x32_bf16 v[100:103], v[160:163], v[194:197], v[100:103]
	v_mfma_f32_16x16x32_bf16 v[88:91], v[152:155], v[208:211], v[88:91]
	v_mfma_f32_16x16x32_bf16 v[84:87], v[160:163], v[208:211], v[84:87]
	v_mfma_f32_16x16x32_bf16 v[72:75], v[152:155], v[216:219], v[72:75]
	v_mfma_f32_16x16x32_bf16 v[68:71], v[160:163], v[216:219], v[68:71]
	s_setprio 0
	s_barrier
; #define PG8_STAGE(bufoff, gbase, voff) do { _Pragma("unroll") for (int _i = 0; _i < 2; ++_i) \
;         __builtin_amdgcn_global_load_lds((const unsigned*)((const char*)(gbase) + (voff)[_i]), (PG8_LAS unsigned*)(lds + (bufoff) + ldsw + _i * 8192), 16, 0, 0); } while (0)
; #define PG8_LDA(dst, b, h) do { _Pragma("unroll") for (int m = 0; m < 4; ++m) _Pragma("unroll") for (int k = 0; k < 2; ++k) dst[m][k] = *(const PG8_LAS bf16x8*)(lds + PG8_SA(b, h) + aoff + m * 2048 + k * 1024); } while (0)
; #define PG8_LDB(dst, b, h) do { _Pragma("unroll") for (int n = 0; n < 2; ++n) _Pragma("unroll") for (int k = 0; k < 2; ++k) dst[n][k] = *(const PG8_LAS bf16x8*)(lds + PG8_SB(b, h) + boff + n * 2048 + k * 1024); } while (0)
; #define PG8_MMA(ai, bj, At, Bt) do { __builtin_amdgcn_s_setprio(1); _Pragma("unroll") for (int m = 0; m < 4; ++m) _Pragma("unroll") for (int n = 0; n < 2; ++n) _Pragma("unroll") for (int k = 0; k < 2; ++k) \
;         acc[ai][bj][m][n] = __builtin_amdgcn_mfma_f32_16x16x32_bf16(Bt[n][k], At[m][k], acc[ai][bj][m][n], 0, 0, 0); __builtin_amdgcn_s_setprio(0); } while (0)
; #define PG8_WAIT_V(n) asm volatile("s_waitcnt vmcnt(" #n ")" ::: "memory")
; #define PG8_WAIT_L(n) asm volatile("s_waitcnt lgkmcnt(" #n ")" ::: "memory")
; #define PG8_BAR __builtin_amdgcn_s_barrier()
; #define PG8_SCHED __builtin_amdgcn_sched_barrier(0)
; template <class Epi, class Sched, bool ALIGN_EPI = false, bool SP2 = false>
; __device__ __forceinline__ void gemm_phase(PG8_LAS unsigned char* lds, const Gemm g, const Sched& S, const Epi& E) {
;     ...
;             PG8_LDB(B0, 1, 0); PG8_LDB(B1, 1, 1); PG8_SCHED; PG8_LDA(At, 1, 0); PG8_STAGE(PG8_SA(0, 1), a2 + hstep, voffA);
;             PG8_WAIT_V(8); PG8_WAIT_L(0); PG8_BAR; PG8_MMA(0, 0, At, B0); PG8_MMA(0, 1, At, B1); PG8_BAR; PG8_SCHED;
;             PG8_LDA(At, 1, 1); PG8_STAGE(PG8_SB(1, 0), b3, voffB); PG8_STAGE(PG8_SB(1, 1), b3 + hstep, voffB); PG8_STAGE(PG8_SA(1, 0), a3, voffA);
;             PG8_WAIT_V(8); PG8_WAIT_L(0); PG8_BAR; if (cur.half == 0) { PG8_MMA(1, 0, At, B0); PG8_MMA(1, 1, At, B1); } PG8_BAR; PG8_SCHED;
	s_add_i32 s10, s61, s27
	v_lshl_add_u64 v[228:229], v[228:229], 0, s[42:43]
	s_mov_b32 m0, s10
	ds_read_b128 v[182:185], v206 offset:49152
	ds_read_b128 v[186:189], v206 offset:50176
	ds_read_b128 v[190:193], v206 offset:51200
	ds_read_b128 v[194:197], v206 offset:52224
	ds_read_b128 v[198:201], v206 offset:53248
	ds_read_b128 v[208:211], v206 offset:54272
	ds_read_b128 v[212:215], v206 offset:55296
	ds_read_b128 v[216:219], v206 offset:56320
	global_load_lds_dwordx4 v[228:229], off
	s_add_i32 m0, s10, 0x2000
	s_add_u32 s0, s0, 0x40080
	v_lshl_add_u64 v[228:229], v[230:231], 0, s[42:43]
	s_addc_u32 s1, s1, 0
	s_add_i32 s10, s63, s27
	global_load_lds_dwordx4 v[228:229], off
	v_lshl_add_u64 v[228:229], s[0:1], 0, v[166:167]
	s_mov_b32 m0, s10
	s_nop 0
	global_load_lds_dwordx4 v[228:229], off
	v_lshl_add_u64 v[228:229], s[0:1], 0, v[170:171]
	s_add_i32 m0, s10, 0x2000
	s_nop 0
	global_load_lds_dwordx4 v[228:229], off
	v_lshl_add_u64 v[228:229], v[232:233], 0, s[42:43]
	s_mov_b32 m0, s41
	s_nop 0
	global_load_lds_dwordx4 v[228:229], off
	v_lshl_add_u64 v[228:229], v[234:235], 0, s[42:43]
	s_mov_b32 m0, s71
	s_nop 0
	global_load_lds_dwordx4 v[228:229], off
	s_waitcnt vmcnt(8)
	s_waitcnt lgkmcnt(0)
	s_barrier
	s_setprio 1
	s_waitcnt lgkmcnt(0)
	v_mfma_f32_16x16x32_bf16 v[64:67], v[132:135], v[182:185], v[64:67]
	v_mfma_f32_16x16x32_bf16 v[60:63], v[140:143], v[182:185], v[60:63]
	v_mfma_f32_16x16x32_bf16 v[48:51], v[132:135], v[190:193], v[48:51]
	v_mfma_f32_16x16x32_bf16 v[44:47], v[140:143], v[190:193], v[44:47]
	v_mfma_f32_16x16x32_bf16 v[32:35], v[132:135], v[198:201], v[32:35]
	v_mfma_f32_16x16x32_bf16 v[28:31], v[140:143], v[198:201], v[28:31]
	v_mfma_f32_16x16x32_bf16 v[16:19], v[132:135], v[212:215], v[16:19]
	v_mfma_f32_16x16x32_bf16 v[12:15], v[140:143], v[212:215], v[12:15]
	v_mfma_f32_16x16x32_bf16 v[64:67], v[136:139], v[186:189], v[64:67]
	v_mfma_f32_16x16x32_bf16 v[60:63], v[144:147], v[186:189], v[60:63]
	v_mfma_f32_16x16x32_bf16 v[48:51], v[136:139], v[194:197], v[48:51]
	v_mfma_f32_16x16x32_bf16 v[44:47], v[144:147], v[194:197], v[44:47]
	v_mfma_f32_16x16x32_bf16 v[32:35], v[136:139], v[208:211], v[32:35]
	v_mfma_f32_16x16x32_bf16 v[28:31], v[144:147], v[208:211], v[28:31]
	v_mfma_f32_16x16x32_bf16 v[16:19], v[136:139], v[216:219], v[16:19]
	v_mfma_f32_16x16x32_bf16 v[12:15], v[144:147], v[216:219], v[12:15]
	s_setprio 0
	s_setprio 1
	v_mfma_f32_16x16x32_bf16 v[56:59], v[148:151], v[182:185], v[56:59]
	v_mfma_f32_16x16x32_bf16 v[52:55], v[156:159], v[182:185], v[52:55]
	v_mfma_f32_16x16x32_bf16 v[40:43], v[148:151], v[190:193], v[40:43]
	v_mfma_f32_16x16x32_bf16 v[36:39], v[156:159], v[190:193], v[36:39]
	v_mfma_f32_16x16x32_bf16 v[24:27], v[148:151], v[198:201], v[24:27]
	v_mfma_f32_16x16x32_bf16 v[20:23], v[156:159], v[198:201], v[20:23]
	v_mfma_f32_16x16x32_bf16 v[8:11], v[148:151], v[212:215], v[8:11]
	v_mfma_f32_16x16x32_bf16 v[4:7], v[156:159], v[212:215], v[4:7]
	v_mfma_f32_16x16x32_bf16 v[56:59], v[152:155], v[186:189], v[56:59]
	v_mfma_f32_16x16x32_bf16 v[52:55], v[160:163], v[186:189], v[52:55]
	v_mfma_f32_16x16x32_bf16 v[40:43], v[152:155], v[194:197], v[40:43]
	v_mfma_f32_16x16x32_bf16 v[36:39], v[160:163], v[194:197], v[36:39]
	v_mfma_f32_16x16x32_bf16 v[24:27], v[152:155], v[208:211], v[24:27]
	v_mfma_f32_16x16x32_bf16 v[20:23], v[160:163], v[208:211], v[20:23]
	v_mfma_f32_16x16x32_bf16 v[8:11], v[152:155], v[216:219], v[8:11]
	v_mfma_f32_16x16x32_bf16 v[4:7], v[160:163], v[216:219], v[4:7]
	s_setprio 0
	s_barrier
	s_add_i32 s39, s39, 2
	s_add_u32 s8, s8, 0x100
	s_addc_u32 s9, s9, 0
	s_add_u32 s36, s36, 0x100
	s_addc_u32 s38, s38, 0
	s_cmp_gt_u32 s39, 13
	s_cbranch_scc0 .LBB0_395
	s_and_b64 vcc, exec, s[58:59]
	s_cbranch_vccz .LBB0_398
	s_barrier

; #define PG8_LAS __attribute__((address_space(3)))
;     __device__ bool next(int i, Unit& u) const { if (!base.next(i >> 1, u)) return false; if (i & 1) { u.pm += MTOK / BM; u.pn += DM / BM; } return true; }
; template <class Epi, class Sched, bool ALIGN_EPI = false, bool SP2 = false>
; __device__ __forceinline__ void gemm_phase(PG8_LAS unsigned char* lds, const Gemm g, const Sched& S, const Epi& E) {
;     ...
;     for (int i = 0; i < 2; ++i) { int R, C; stage_rc(tid * 16 + i * 8192, R, C); const int Rb = Epi::PERM ? ((R & ~31) + perm32(R & 31)) : R;
;         voffA[i] = (unsigned)(R * K + C) * 2u; voffB[i] = (unsigned)(Rb * K + C) * 2u; }
;     const size_t kstep = (size_t)(BK * 2);
;     const size_t hstep = (size_t)HALF * K * 2;
;     const size_t tstep = 2 * hstep;
;     const unsigned ldsw = (unsigned)wid * 1024u;
;     const int aoff = lds_byte(wr * 64 + fr, fq * 8), boff = lds_byte(wc * 32 + fr, fq * 8);
;     ...
;     Unit cur, nxt; int ui = 0;
;     ...
;     unsigned pg8_probe_acc = 0u;
;     ...
;     if (!S.next(0, cur)) return;
;     ...
;     const unsigned long long tramp_ = __builtin_amdgcn_s_memrealtime();
;     ...
;     static_assert(!Epi::ROWSCALE || SP2, "row factors are staged in the SP2 prologue");
;     f32x4 rowp_ = {0.f, 0.f, 0.f, 0.f}; if constexpr (Epi::ROWSCALE) rowp_ = load_row_partials(E.rsp, cur.pm, tid);
;     f32x4 acc[2][2][4][2];
; #pragma unroll
;     for (int a = 0; a < 2; ++a)
; #pragma unroll
;         for (int b = 0; b < 2; ++b)
; #pragma unroll
;             for (int m = 0; m < 4; ++m)
; #pragma unroll
;                 for (int n = 0; n < 2; ++n) acc[a][b][m][n] = (f32x4){0.f, 0.f, 0.f, 0.f};
;     bf16x8 At[4][2], B0[2][2], B1[2][2];
;     const char* cA = (const char*)g.A + (size_t)cur.pm * tstep + (cur.half == 2 ? hstep : (size_t)0); const char* cB = (const char*)g.Bt + (size_t)cur.pn * tstep;
;     S.a_ready(cur);
;     if constexpr (SP2) {
;         PG8_STAGE(PG8_SB(0, 0), cB, voffB); PG8_STAGE(PG8_SB(0, 1), cB + hstep, voffB); PG8_STAGE(PG8_SA(0, 0), cA, voffA); PG8_STAGE(PG8_SA(0, 1), cA + hstep, voffA);
;         if (wr == 1) PG8_BAR;
;         PG8_WAIT_V(2); PG8_BAR;
;         if constexpr (Epi::ROWSCALE) stage_row_factors(rowp_, (PG8_LAS float*)E.rsl, tid);
;         PG8_STAGE(PG8_SB(1, 0), cB + kstep, voffB); PG8_STAGE(PG8_SA(1, 0), cA + kstep, voffA); PG8_STAGE(PG8_SB(1, 1), cB + hstep + kstep, voffB);
;         PG8_WAIT_V(6); PG8_BAR;
.LBB0_1125:
	s_add_u32 s34, s12, 0x10000000
	s_addc_u32 s35, s13, 0
	s_add_u32 s10, s12, 0x11000000
	s_addc_u32 s11, s13, 0
	s_add_u32 s12, s12, 0x12000000
	s_addc_u32 s13, s13, 0
	s_lshl_b32 s5, s18, 5
	s_and_b32 s5, s5, 0x60
	s_add_i32 m0, s28, 0x18000
	v_lshl_add_u64 v[10:11], v[10:11], 0, s[42:43]
	s_lshl_b32 s1, s17, 13
	s_waitcnt lgkmcnt(0)
	s_lshl_b32 s20, s5, 7
	s_waitcnt vmcnt(2)
	s_barrier
	global_load_lds_dwordx4 v[10:11], off
	v_lshl_add_u64 v[8:9], v[8:9], 0, s[42:43]
	s_add_i32 m0, s28, 0x1a000
	s_add_i32 s36, s28, 0x8000
	s_add_i32 s40, s28, 0xa000
	global_load_lds_dwordx4 v[8:9], off
	v_lshl_add_u64 v[4:5], v[4:5], 0, s[42:43]
	s_mov_b32 m0, s36
	s_add_u32 s18, s14, 0x20080
	global_load_lds_dwordx4 v[4:5], off
	v_lshl_add_u64 v[4:5], v[6:7], 0, s[42:43]
	s_mov_b32 m0, s40
	s_addc_u32 s19, s15, 0
	global_load_lds_dwordx4 v[4:5], off
	s_add_i32 m0, s28, 0x1c000
	v_lshl_add_u64 v[4:5], s[18:19], 0, v[2:3]
	global_load_lds_dwordx4 v[4:5], off
	v_lshl_add_u64 v[4:5], s[18:19], 0, v[168:169]
	s_add_i32 m0, s28, 0x1e000
	v_mov_b32_e32 v7, v3
	global_load_lds_dwordx4 v[4:5], off
	v_lshrrev_b32_e32 v5, 1, v12
	v_and_b32_e32 v5, 24, v5
	v_and_b32_e32 v4, 15, v12
	v_lshlrev_b32_e32 v6, 1, v5
	v_lshl_or_b32 v200, s17, 6, v4
	v_lshl_or_b32 v4, v4, 6, v6
	v_lshlrev_b32_e32 v6, 2, v12
	v_and_b32_e32 v6, 32, v6
	v_bitop3_b32 v8, v4, s1, v6 bitop3:0xde
	v_bitop3_b32 v201, v4, s20, v6 bitop3:0xde
	v_lshlrev_b32_e32 v4, 13, v13
	v_and_b32_e32 v4, 0xffffc000, v4
	v_or_b32_e32 v202, s5, v5
	v_lshl_add_u32 v4, v14, 10, v4
	v_and_b32_e32 v5, 1, v13
	v_lshl_or_b32 v4, v5, 6, v4
	v_lshl_add_u32 v170, v15, 1, v4
	v_lshlrev_b32_e32 v4, 13, v16
	v_and_b32_e32 v4, 0xffffc000, v4
	v_lshl_add_u32 v4, v17, 10, v4
	v_and_b32_e32 v5, 1, v16
	s_waitcnt vmcnt(6)
	v_lshl_or_b32 v4, v5, 6, v4
	v_mov_b32_e32 v6, v3
	s_cmpk_lt_u32 s16, 0x100
	v_lshl_add_u32 v172, v18, 1, v4
	v_mov_b32_e32 v4, v3
	v_mov_b32_e32 v5, v3
	v_add_u32_e32 v203, 0, v8
	v_mov_b64_e32 v[10:11], v[6:7]
	v_mov_b64_e32 v[22:23], v[6:7]
	v_mov_b64_e32 v[26:27], v[6:7]
	v_mov_b64_e32 v[46:47], v[6:7]
	v_mov_b64_e32 v[50:51], v[6:7]
	v_mov_b64_e32 v[78:79], v[6:7]
	v_mov_b64_e32 v[82:83], v[6:7]
	v_mov_b64_e32 v[14:15], v[6:7]
	v_mov_b64_e32 v[18:19], v[6:7]
	v_mov_b64_e32 v[30:31], v[6:7]
	v_mov_b64_e32 v[34:35], v[6:7]
	v_mov_b64_e32 v[62:63], v[6:7]
	v_mov_b64_e32 v[66:67], v[6:7]
	v_mov_b64_e32 v[94:95], v[6:7]
	v_mov_b64_e32 v[98:99], v[6:7]
	v_mov_b64_e32 v[110:111], v[6:7]
	v_mov_b64_e32 v[114:115], v[6:7]
	v_mov_b64_e32 v[142:143], v[6:7]
	v_mov_b64_e32 v[146:147], v[6:7]
	v_mov_b64_e32 v[150:151], v[6:7]
	v_mov_b64_e32 v[154:155], v[6:7]
	v_mov_b64_e32 v[158:159], v[6:7]
	v_mov_b64_e32 v[162:163], v[6:7]
	v_mov_b64_e32 v[126:127], v[6:7]
	v_mov_b64_e32 v[130:131], v[6:7]
	v_mov_b64_e32 v[118:119], v[6:7]
	v_mov_b64_e32 v[122:123], v[6:7]
	v_mov_b64_e32 v[86:87], v[6:7]
	v_mov_b64_e32 v[90:91], v[6:7]
	v_mov_b64_e32 v[54:55], v[6:7]
	v_mov_b64_e32 v[58:59], v[6:7]
	s_cselect_b64 s[16:17], -1, 0
	v_mov_b32_e32 v171, v3
	v_mov_b32_e32 v173, v3
	s_mov_b32 s1, 0
	v_mov_b64_e32 v[8:9], v[4:5]
	v_mov_b64_e32 v[20:21], v[4:5]
	v_mov_b64_e32 v[24:25], v[4:5]
	v_mov_b64_e32 v[44:45], v[4:5]
	v_mov_b64_e32 v[48:49], v[4:5]
	v_mov_b64_e32 v[76:77], v[4:5]
	v_mov_b64_e32 v[80:81], v[4:5]
	v_mov_b64_e32 v[12:13], v[4:5]
	v_mov_b64_e32 v[16:17], v[4:5]
	v_mov_b64_e32 v[28:29], v[4:5]
	v_mov_b64_e32 v[32:33], v[4:5]
	v_mov_b64_e32 v[60:61], v[4:5]
	v_mov_b64_e32 v[64:65], v[4:5]
	v_mov_b64_e32 v[92:93], v[4:5]
	v_mov_b64_e32 v[96:97], v[4:5]
	v_mov_b64_e32 v[108:109], v[4:5]
	v_mov_b64_e32 v[112:113], v[4:5]
	v_mov_b64_e32 v[140:141], v[4:5]
	v_mov_b64_e32 v[144:145], v[4:5]
	v_mov_b64_e32 v[148:149], v[4:5]
	v_mov_b64_e32 v[152:153], v[4:5]
	v_mov_b64_e32 v[156:157], v[4:5]
	v_mov_b64_e32 v[160:161], v[4:5]
	v_mov_b64_e32 v[124:125], v[4:5]
	v_mov_b64_e32 v[128:129], v[4:5]
	v_mov_b64_e32 v[116:117], v[4:5]
	v_mov_b64_e32 v[120:121], v[4:5]
	v_mov_b64_e32 v[84:85], v[4:5]
	v_mov_b64_e32 v[88:89], v[4:5]
	v_mov_b64_e32 v[52:53], v[4:5]
	v_mov_b64_e32 v[56:57], v[4:5]
	s_barrier
	s_branch .LBB0_1128
	.p2align 6
	s_nop 0
	s_nop 0
	s_nop 0
	s_nop 0
	s_nop 0
	s_nop 0
	s_nop 0
.LBB0_1126:
	s_mov_b64 s[0:1], 0

;     __device__ __forceinline__ void a_ready(const Unit&) const { if (++ncall == 3 && sig != nullptr && threadIdx.x == 0) __hip_atomic_fetch_add(sig, 1u, __ATOMIC_RELAXED, __HIP_MEMORY_SCOPE_AGENT); }
; #define PG8_STAGE(bufoff, gbase, voff) do { _Pragma("unroll") for (int _i = 0; _i < 2; ++_i) \
;         __builtin_amdgcn_global_load_lds((const unsigned*)((const char*)(gbase) + (voff)[_i]), (PG8_LAS unsigned*)(lds + (bufoff) + ldsw + _i * 8192), 16, 0, 0); } while (0)
; #define PG8_LDA(dst, b, h) do { _Pragma("unroll") for (int m = 0; m < 4; ++m) _Pragma("unroll") for (int k = 0; k < 2; ++k) dst[m][k] = *(const PG8_LAS bf16x8*)(lds + PG8_SA(b, h) + aoff + m * 2048 + k * 1024); } while (0)
; #define PG8_BAR __builtin_amdgcn_s_barrier()
; template <class Epi, class Sched, bool ALIGN_EPI = false, bool SP2 = false>
; __device__ __forceinline__ void gemm_phase(PG8_LAS unsigned char* lds, const Gemm g, const Sched& S, const Epi& E) {
;     ...
;         for (int t = 0; t < nt; t += 2) {
;             const bool last = (t == nt - 2);
;             const char* a1 = cA + (size_t)(t + 1) * kstep;
;             const char* a2 = last ? nA : cA + (size_t)(t + 2) * kstep; const char* b2 = last ? nB : cB + (size_t)(t + 2) * kstep;
;             const char* a3 = a2 + kstep; const char* b3 = b2 + kstep;
;             if (last && has_next) S.a_ready(nxt);
;             if constexpr (SP2) {
;             PG8_LDB(B0, 0, 0); PG8_LDB(B1, 0, 1); PG8_SCHED; PG8_LDA(At, 0, 0); PG8_STAGE(PG8_SA(1, 1), a1 + hstep, voffA);
;     ...
;             if (PROBE_KIND == 18 && t == 0 && ui > 0 && g.probe) { const unsigned long long tq_ = __builtin_amdgcn_s_memrealtime(); PG8_WAIT_V(8); pg8_probe_acc += (unsigned)(__builtin_amdgcn_s_memrealtime() - tq_); }
;     ...
;             PG8_WAIT_V(8); PG8_WAIT_L(0); PG8_BAR; PG8_MMA(0, 0, At, B0); PG8_MMA(0, 1, At, B1); PG8_BAR; PG8_SCHED;
;             PG8_LDA(At, 0, 1); PG8_STAGE(PG8_SB(0, 0), b2, voffB); PG8_STAGE(PG8_SB(0, 1), b2 + hstep, voffB); PG8_STAGE(PG8_SA(0, 0), a2, voffA);
;             PG8_WAIT_V(8); PG8_WAIT_L(0); PG8_BAR; if (cur.half == 0) { PG8_MMA(1, 0, At, B0); PG8_MMA(1, 1, At, B1); } PG8_BAR; PG8_SCHED;
;             PG8_LDB(B0, 1, 0); PG8_LDB(B1, 1, 1); PG8_SCHED; PG8_LDA(At, 1, 0); PG8_STAGE(PG8_SA(0, 1), a2 + hstep, voffA);
;             PG8_WAIT_V(8); PG8_WAIT_L(0); PG8_BAR; PG8_MMA(0, 0, At, B0); PG8_MMA(0, 1, At, B1); PG8_BAR; PG8_SCHED;
.LBB0_1135:
	s_add_u32 s14, s6, 0xfffe0080
	s_addc_u32 s15, s7, -1
	s_add_i32 s65, 0, 0x10000
	s_cmp_eq_u32 s64, 4
	s_cselect_b32 s21, s1, s15
	s_cselect_b32 s20, s5, s14
	s_cselect_b32 s15, s19, s63
	s_cselect_b32 s14, s39, s62
	s_add_i32 s68, 0, 0x14000
	v_add_u32_e32 v72, s65, v201
	v_add_u32_e32 v136, s68, v201
	ds_read_b128 v[36:39], v72
	ds_read_b128 v[40:43], v72 offset:1024
	ds_read_b128 v[68:71], v72 offset:2048
	ds_read_b128 v[72:75], v72 offset:3072
	ds_read_b128 v[100:103], v136
	ds_read_b128 v[104:107], v136 offset:1024
	ds_read_b128 v[132:135], v136 offset:2048
	ds_read_b128 v[136:139], v136 offset:3072
	v_lshl_add_u64 v[198:199], s[6:7], 0, v[170:171]
	s_add_i32 m0, s28, 0xc000
	ds_read_b128 v[174:177], v203
	ds_read_b128 v[178:181], v203 offset:1024
	ds_read_b128 v[182:185], v203 offset:2048
	ds_read_b128 v[186:189], v203 offset:3072
	ds_read_b128 v[190:193], v203 offset:4096
	ds_read_b128 v[194:197], v203 offset:5120
	ds_read_b128 v[204:207], v203 offset:6144
	ds_read_b128 v[208:211], v203 offset:7168
	global_load_lds_dwordx4 v[198:199], off
	v_lshl_add_u64 v[198:199], s[6:7], 0, v[172:173]
	s_add_i32 m0, s28, 0xe000
	s_nop 0
	global_load_lds_dwordx4 v[198:199], off
	s_waitcnt vmcnt(8)
	s_waitcnt lgkmcnt(0)
	s_barrier
	s_setprio 1
	s_waitcnt lgkmcnt(0)
	v_mfma_f32_16x16x32_bf16 v[56:59], v[36:39], v[174:177], v[56:59]
	v_mfma_f32_16x16x32_bf16 v[52:55], v[68:71], v[174:177], v[52:55]
	v_mfma_f32_16x16x32_bf16 v[88:91], v[36:39], v[182:185], v[88:91]
	v_mfma_f32_16x16x32_bf16 v[84:87], v[68:71], v[182:185], v[84:87]
	v_mfma_f32_16x16x32_bf16 v[120:123], v[36:39], v[190:193], v[120:123]
	v_mfma_f32_16x16x32_bf16 v[116:119], v[68:71], v[190:193], v[116:119]
	v_mfma_f32_16x16x32_bf16 v[128:131], v[36:39], v[204:207], v[128:131]
	v_mfma_f32_16x16x32_bf16 v[124:127], v[68:71], v[204:207], v[124:127]
	v_mfma_f32_16x16x32_bf16 v[56:59], v[40:43], v[178:181], v[56:59]
	v_mfma_f32_16x16x32_bf16 v[52:55], v[72:75], v[178:181], v[52:55]
	v_mfma_f32_16x16x32_bf16 v[88:91], v[40:43], v[186:189], v[88:91]
	v_mfma_f32_16x16x32_bf16 v[84:87], v[72:75], v[186:189], v[84:87]
	v_mfma_f32_16x16x32_bf16 v[120:123], v[40:43], v[194:197], v[120:123]
	v_mfma_f32_16x16x32_bf16 v[116:119], v[72:75], v[194:197], v[116:119]
	v_mfma_f32_16x16x32_bf16 v[128:131], v[40:43], v[208:211], v[128:131]
	v_mfma_f32_16x16x32_bf16 v[124:127], v[72:75], v[208:211], v[124:127]
	s_setprio 0
	s_setprio 1
	v_mfma_f32_16x16x32_bf16 v[160:163], v[100:103], v[174:177], v[160:163]
	v_mfma_f32_16x16x32_bf16 v[156:159], v[132:135], v[174:177], v[156:159]
	v_mfma_f32_16x16x32_bf16 v[152:155], v[100:103], v[182:185], v[152:155]
	v_mfma_f32_16x16x32_bf16 v[148:151], v[132:135], v[182:185], v[148:151]
	v_mfma_f32_16x16x32_bf16 v[144:147], v[100:103], v[190:193], v[144:147]
	v_mfma_f32_16x16x32_bf16 v[140:143], v[132:135], v[190:193], v[140:143]
	v_mfma_f32_16x16x32_bf16 v[112:115], v[100:103], v[204:207], v[112:115]
	v_mfma_f32_16x16x32_bf16 v[108:111], v[132:135], v[204:207], v[108:111]
	v_mfma_f32_16x16x32_bf16 v[160:163], v[104:107], v[178:181], v[160:163]
	v_mfma_f32_16x16x32_bf16 v[156:159], v[136:139], v[178:181], v[156:159]
	v_mfma_f32_16x16x32_bf16 v[152:155], v[104:107], v[186:189], v[152:155]
	v_mfma_f32_16x16x32_bf16 v[148:151], v[136:139], v[186:189], v[148:151]
	v_mfma_f32_16x16x32_bf16 v[144:147], v[104:107], v[194:197], v[144:147]
	v_mfma_f32_16x16x32_bf16 v[140:143], v[136:139], v[194:197], v[140:143]
	v_mfma_f32_16x16x32_bf16 v[112:115], v[104:107], v[208:211], v[112:115]
	v_mfma_f32_16x16x32_bf16 v[108:111], v[136:139], v[208:211], v[108:111]
	s_setprio 0
	s_barrier
	s_add_i32 s65, s65, s27
	v_lshl_add_u64 v[198:199], s[14:15], 0, v[2:3]
	s_mov_b32 m0, s65
	ds_read_b128 v[174:177], v203 offset:16384
	ds_read_b128 v[178:181], v203 offset:17408
	ds_read_b128 v[182:185], v203 offset:18432
	ds_read_b128 v[186:189], v203 offset:19456
	ds_read_b128 v[190:193], v203 offset:20480
	ds_read_b128 v[194:197], v203 offset:21504
	ds_read_b128 v[204:207], v203 offset:22528
	ds_read_b128 v[208:211], v203 offset:23552
	global_load_lds_dwordx4 v[198:199], off
	s_add_i32 m0, s65, 0x2000
	s_add_u32 s66, s14, 0x20000
	v_lshl_add_u64 v[212:213], s[14:15], 0, v[168:169]
	s_addc_u32 s67, s15, 0
	s_add_i32 s65, s68, s27
	global_load_lds_dwordx4 v[212:213], off
	v_lshl_add_u64 v[214:215], s[66:67], 0, v[2:3]
	s_mov_b32 m0, s65
	v_lshl_add_u64 v[216:217], s[20:21], 0, v[166:167]
	global_load_lds_dwordx4 v[214:215], off
	v_lshl_add_u64 v[214:215], s[66:67], 0, v[168:169]
	s_add_i32 m0, s65, 0x2000
	s_nop 0
	global_load_lds_dwordx4 v[214:215], off
	v_lshl_add_u64 v[214:215], s[20:21], 0, v[164:165]
	s_mov_b32 m0, s28
	s_nop 0
	global_load_lds_dwordx4 v[214:215], off
	s_mov_b32 m0, s29
	s_nop 0
	global_load_lds_dwordx4 v[216:217], off
	s_nop 0
	s_waitcnt vmcnt(8)
	s_waitcnt lgkmcnt(0)
	s_barrier
; #define PG8_STAGE(bufoff, gbase, voff) do { _Pragma("unroll") for (int _i = 0; _i < 2; ++_i) \
;         __builtin_amdgcn_global_load_lds((const unsigned*)((const char*)(gbase) + (voff)[_i]), (PG8_LAS unsigned*)(lds + (bufoff) + ldsw + _i * 8192), 16, 0, 0); } while (0)
; #define PG8_LDA(dst, b, h) do { _Pragma("unroll") for (int m = 0; m < 4; ++m) _Pragma("unroll") for (int k = 0; k < 2; ++k) dst[m][k] = *(const PG8_LAS bf16x8*)(lds + PG8_SA(b, h) + aoff + m * 2048 + k * 1024); } while (0)
; #define PG8_LDB(dst, b, h) do { _Pragma("unroll") for (int n = 0; n < 2; ++n) _Pragma("unroll") for (int k = 0; k < 2; ++k) dst[n][k] = *(const PG8_LAS bf16x8*)(lds + PG8_SB(b, h) + boff + n * 2048 + k * 1024); } while (0)
; #define PG8_MMA(ai, bj, At, Bt) do { __builtin_amdgcn_s_setprio(1); _Pragma("unroll") for (int m = 0; m < 4; ++m) _Pragma("unroll") for (int n = 0; n < 2; ++n) _Pragma("unroll") for (int k = 0; k < 2; ++k) \
;         acc[ai][bj][m][n] = __builtin_amdgcn_mfma_f32_16x16x32_bf16(Bt[n][k], At[m][k], acc[ai][bj][m][n], 0, 0, 0); __builtin_amdgcn_s_setprio(0); } while (0)
; #define PG8_WAIT_V(n) asm volatile("s_waitcnt vmcnt(" #n ")" ::: "memory")
; #define PG8_WAIT_L(n) asm volatile("s_waitcnt lgkmcnt(" #n ")" ::: "memory")
; #define PG8_BAR __builtin_amdgcn_s_barrier()
; #define PG8_SCHED __builtin_amdgcn_sched_barrier(0)
; template <class Epi, class Sched, bool ALIGN_EPI = false, bool SP2 = false>
; __device__ __forceinline__ void gemm_phase(PG8_LAS unsigned char* lds, const Gemm g, const Sched& S, const Epi& E) {
;     ...
;             PG8_WAIT_V(8); PG8_WAIT_L(0); PG8_BAR; if (cur.half == 0) { PG8_MMA(1, 0, At, B0); PG8_MMA(1, 1, At, B1); } PG8_BAR; PG8_SCHED;
;             PG8_LDB(B0, 1, 0); PG8_LDB(B1, 1, 1); PG8_SCHED; PG8_LDA(At, 1, 0); PG8_STAGE(PG8_SA(0, 1), a2 + hstep, voffA);
;             PG8_WAIT_V(8); PG8_WAIT_L(0); PG8_BAR; PG8_MMA(0, 0, At, B0); PG8_MMA(0, 1, At, B1); PG8_BAR; PG8_SCHED;
	s_setprio 1
	s_waitcnt lgkmcnt(0)
	v_mfma_f32_16x16x32_bf16 v[96:99], v[36:39], v[174:177], v[96:99]
	v_mfma_f32_16x16x32_bf16 v[92:95], v[68:71], v[174:177], v[92:95]
	v_mfma_f32_16x16x32_bf16 v[64:67], v[36:39], v[182:185], v[64:67]
	v_mfma_f32_16x16x32_bf16 v[60:63], v[68:71], v[182:185], v[60:63]
	v_mfma_f32_16x16x32_bf16 v[32:35], v[36:39], v[190:193], v[32:35]
	v_mfma_f32_16x16x32_bf16 v[28:31], v[68:71], v[190:193], v[28:31]
	v_mfma_f32_16x16x32_bf16 v[16:19], v[36:39], v[204:207], v[16:19]
	v_mfma_f32_16x16x32_bf16 v[12:15], v[68:71], v[204:207], v[12:15]
	v_mfma_f32_16x16x32_bf16 v[96:99], v[40:43], v[178:181], v[96:99]
	v_mfma_f32_16x16x32_bf16 v[92:95], v[72:75], v[178:181], v[92:95]
	v_mfma_f32_16x16x32_bf16 v[64:67], v[40:43], v[186:189], v[64:67]
	v_mfma_f32_16x16x32_bf16 v[60:63], v[72:75], v[186:189], v[60:63]
	v_mfma_f32_16x16x32_bf16 v[32:35], v[40:43], v[194:197], v[32:35]
	v_mfma_f32_16x16x32_bf16 v[28:31], v[72:75], v[194:197], v[28:31]
	v_mfma_f32_16x16x32_bf16 v[16:19], v[40:43], v[208:211], v[16:19]
	v_mfma_f32_16x16x32_bf16 v[12:15], v[72:75], v[208:211], v[12:15]
	s_setprio 0
	s_setprio 1
	v_mfma_f32_16x16x32_bf16 v[48:51], v[100:103], v[182:185], v[48:51]
	v_mfma_f32_16x16x32_bf16 v[44:47], v[132:135], v[182:185], v[44:47]
	v_mfma_f32_16x16x32_bf16 v[24:27], v[100:103], v[190:193], v[24:27]
	v_mfma_f32_16x16x32_bf16 v[20:23], v[132:135], v[190:193], v[20:23]
	v_mfma_f32_16x16x32_bf16 v[8:11], v[100:103], v[204:207], v[8:11]
	v_mfma_f32_16x16x32_bf16 v[4:7], v[132:135], v[204:207], v[4:7]
	v_mfma_f32_16x16x32_bf16 v[36:39], v[100:103], v[174:177], v[80:83]
	v_mfma_f32_16x16x32_bf16 v[40:43], v[132:135], v[174:177], v[76:79]
	v_mfma_f32_16x16x32_bf16 v[48:51], v[104:107], v[186:189], v[48:51]
	v_mfma_f32_16x16x32_bf16 v[44:47], v[136:139], v[186:189], v[44:47]
	v_mfma_f32_16x16x32_bf16 v[24:27], v[104:107], v[194:197], v[24:27]
	v_mfma_f32_16x16x32_bf16 v[20:23], v[136:139], v[194:197], v[20:23]
	v_mfma_f32_16x16x32_bf16 v[8:11], v[104:107], v[208:211], v[8:11]
	v_mfma_f32_16x16x32_bf16 v[4:7], v[136:139], v[208:211], v[4:7]
	v_mfma_f32_16x16x32_bf16 v[36:39], v[104:107], v[178:181], v[36:39]
	v_mfma_f32_16x16x32_bf16 v[40:43], v[136:139], v[178:181], v[40:43]
	s_setprio 0
	s_barrier
	s_add_i32 s65, 0, 0x18000
	s_add_i32 s66, 0, 0x1c000
	v_add_u32_e32 v80, s65, v201
	v_add_u32_e32 v136, s66, v201
	ds_read_b128 v[68:71], v80
	ds_read_b128 v[72:75], v80 offset:1024
	ds_read_b128 v[76:79], v80 offset:2048
	ds_read_b128 v[80:83], v80 offset:3072
	ds_read_b128 v[100:103], v136
	ds_read_b128 v[104:107], v136 offset:1024
	ds_read_b128 v[132:135], v136 offset:2048
	ds_read_b128 v[136:139], v136 offset:3072
	s_add_u32 s20, s20, 0x20000
	s_addc_u32 s21, s21, 0
	s_mov_b32 m0, s30
	v_lshl_add_u64 v[218:219], s[20:21], 0, v[164:165]
	ds_read_b128 v[174:177], v203 offset:32768
	ds_read_b128 v[178:181], v203 offset:33792
	ds_read_b128 v[182:185], v203 offset:34816
	ds_read_b128 v[186:189], v203 offset:35840
	ds_read_b128 v[190:193], v203 offset:36864
	ds_read_b128 v[194:197], v203 offset:37888
	ds_read_b128 v[204:207], v203 offset:38912
	ds_read_b128 v[208:211], v203 offset:39936
	global_load_lds_dwordx4 v[218:219], off
	v_lshl_add_u64 v[218:219], s[20:21], 0, v[166:167]
	s_mov_b32 m0, s31
	s_nop 0
	global_load_lds_dwordx4 v[218:219], off
	s_nop 0
	s_waitcnt vmcnt(8)
	s_waitcnt lgkmcnt(0)
	s_barrier
; #define MG_LOAD(c, buf) do { _Pragma("unroll") for (int m2 = 0; m2 < 2; ++m2) _Pragma("unroll") for (int bj = 0; bj < 2; ++bj) { \
;             const size_t ro = (size_t)(row0 + ((c) >> 1) * HALF + (2 * ((c) & 1) + m2) * 16) * DM + col0 + bj * HALF; ga[buf][m2][bj] = *(const u32x2*)(GAx + (ro & amask)); gb[buf][m2][bj] = *(const u32x2*)(GB + ro); } } while (0)
; #define PG8_STAGE(bufoff, gbase, voff) do { _Pragma("unroll") for (int _i = 0; _i < 2; ++_i) \
;         __builtin_amdgcn_global_load_lds((const unsigned*)((const char*)(gbase) + (voff)[_i]), (PG8_LAS unsigned*)(lds + (bufoff) + ldsw + _i * 8192), 16, 0, 0); } while (0)
; #define PG8_LDA(dst, b, h) do { _Pragma("unroll") for (int m = 0; m < 4; ++m) _Pragma("unroll") for (int k = 0; k < 2; ++k) dst[m][k] = *(const PG8_LAS bf16x8*)(lds + PG8_SA(b, h) + aoff + m * 2048 + k * 1024); } while (0)
; #define PG8_MMA(ai, bj, At, Bt) do { __builtin_amdgcn_s_setprio(1); _Pragma("unroll") for (int m = 0; m < 4; ++m) _Pragma("unroll") for (int n = 0; n < 2; ++n) _Pragma("unroll") for (int k = 0; k < 2; ++k) \
;         acc[ai][bj][m][n] = __builtin_amdgcn_mfma_f32_16x16x32_bf16(Bt[n][k], At[m][k], acc[ai][bj][m][n], 0, 0, 0); __builtin_amdgcn_s_setprio(0); } while (0)
; #define PG8_WAIT_V(n) asm volatile("s_waitcnt vmcnt(" #n ")" ::: "memory")
; #define PG8_WAIT_L(n) asm volatile("s_waitcnt lgkmcnt(" #n ")" ::: "memory")
; #define PG8_BAR __builtin_amdgcn_s_barrier()
; #define PG8_SCHED __builtin_amdgcn_sched_barrier(0)
;     __device__ __forceinline__ void operator()(f32x4 (&acc)[2][2][4][2], const Unit& u, int wr, int wc, int fr, int fq) const {
;     ...
;         MG_LOAD(0, 0); MG_LOAD(1, 1);
; template <class Epi, class Sched, bool ALIGN_EPI = false, bool SP2 = false>
; __device__ __forceinline__ void gemm_phase(PG8_LAS unsigned char* lds, const Gemm g, const Sched& S, const Epi& E) {
;     ...
;             PG8_LDA(At, 1, 1); PG8_STAGE(PG8_SB(1, 0), b3, voffB); PG8_STAGE(PG8_SB(1, 1), b3 + hstep, voffB); PG8_STAGE(PG8_SA(1, 0), a3, voffA);
;             PG8_WAIT_V(8); PG8_WAIT_L(0); PG8_BAR; if (cur.half == 0) { PG8_MMA(1, 0, At, B0); PG8_MMA(1, 1, At, B1); } PG8_BAR; PG8_SCHED;
	s_setprio 1
	s_waitcnt lgkmcnt(0)
	v_mfma_f32_16x16x32_bf16 v[56:59], v[68:71], v[174:177], v[56:59]
	v_mfma_f32_16x16x32_bf16 v[52:55], v[76:79], v[174:177], v[52:55]
	v_mfma_f32_16x16x32_bf16 v[88:91], v[68:71], v[182:185], v[88:91]
	v_mfma_f32_16x16x32_bf16 v[84:87], v[76:79], v[182:185], v[84:87]
	v_mfma_f32_16x16x32_bf16 v[120:123], v[68:71], v[190:193], v[120:123]
	v_mfma_f32_16x16x32_bf16 v[116:119], v[76:79], v[190:193], v[116:119]
	v_mfma_f32_16x16x32_bf16 v[128:131], v[68:71], v[204:207], v[128:131]
	v_mfma_f32_16x16x32_bf16 v[124:127], v[76:79], v[204:207], v[124:127]
	v_mfma_f32_16x16x32_bf16 v[56:59], v[72:75], v[178:181], v[56:59]
	v_mfma_f32_16x16x32_bf16 v[52:55], v[80:83], v[178:181], v[52:55]
	v_mfma_f32_16x16x32_bf16 v[88:91], v[72:75], v[186:189], v[88:91]
	v_mfma_f32_16x16x32_bf16 v[84:87], v[80:83], v[186:189], v[84:87]
	v_mfma_f32_16x16x32_bf16 v[120:123], v[72:75], v[194:197], v[120:123]
	v_mfma_f32_16x16x32_bf16 v[116:119], v[80:83], v[194:197], v[116:119]
	v_mfma_f32_16x16x32_bf16 v[128:131], v[72:75], v[208:211], v[128:131]
	v_mfma_f32_16x16x32_bf16 v[124:127], v[80:83], v[208:211], v[124:127]
	s_setprio 0
	s_setprio 1
	v_mfma_f32_16x16x32_bf16 v[160:163], v[100:103], v[174:177], v[160:163]
	v_mfma_f32_16x16x32_bf16 v[156:159], v[132:135], v[174:177], v[156:159]
	v_mfma_f32_16x16x32_bf16 v[152:155], v[100:103], v[182:185], v[152:155]
	v_mfma_f32_16x16x32_bf16 v[148:151], v[132:135], v[182:185], v[148:151]
	v_mfma_f32_16x16x32_bf16 v[144:147], v[100:103], v[190:193], v[144:147]
	v_mfma_f32_16x16x32_bf16 v[140:143], v[132:135], v[190:193], v[140:143]
	v_mfma_f32_16x16x32_bf16 v[112:115], v[100:103], v[204:207], v[112:115]
	v_mfma_f32_16x16x32_bf16 v[108:111], v[132:135], v[204:207], v[108:111]
	v_mfma_f32_16x16x32_bf16 v[160:163], v[104:107], v[178:181], v[160:163]
	v_mfma_f32_16x16x32_bf16 v[156:159], v[136:139], v[178:181], v[156:159]
	v_mfma_f32_16x16x32_bf16 v[152:155], v[104:107], v[186:189], v[152:155]
	v_mfma_f32_16x16x32_bf16 v[148:151], v[136:139], v[186:189], v[148:151]
	v_mfma_f32_16x16x32_bf16 v[144:147], v[104:107], v[194:197], v[144:147]
	v_mfma_f32_16x16x32_bf16 v[140:143], v[136:139], v[194:197], v[140:143]
	v_mfma_f32_16x16x32_bf16 v[112:115], v[104:107], v[208:211], v[112:115]
	v_mfma_f32_16x16x32_bf16 v[108:111], v[136:139], v[208:211], v[108:111]
	s_setprio 0
	s_barrier
	s_add_i32 s20, s65, s27
	v_lshl_add_u64 v[198:199], v[198:199], 0, s[42:43]
	s_mov_b32 m0, s20
	ds_read_b128 v[174:177], v203 offset:49152
	ds_read_b128 v[178:181], v203 offset:50176
	ds_read_b128 v[182:185], v203 offset:51200
	ds_read_b128 v[186:189], v203 offset:52224
	ds_read_b128 v[190:193], v203 offset:53248
	ds_read_b128 v[194:197], v203 offset:54272
	ds_read_b128 v[204:207], v203 offset:55296
	ds_read_b128 v[208:211], v203 offset:56320
	global_load_lds_dwordx4 v[198:199], off
	s_add_i32 m0, s20, 0x2000
	s_add_u32 s14, s14, 0x20080
	v_lshl_add_u64 v[198:199], v[212:213], 0, s[42:43]
	s_addc_u32 s15, s15, 0
	s_add_i32 s20, s66, s27
	global_load_lds_dwordx4 v[198:199], off
	v_lshl_add_u64 v[198:199], s[14:15], 0, v[2:3]
	s_mov_b32 m0, s20
	s_nop 0
	global_load_lds_dwordx4 v[198:199], off
	v_lshl_add_u64 v[198:199], s[14:15], 0, v[168:169]
	s_add_i32 m0, s20, 0x2000
	s_nop 0
	global_load_lds_dwordx4 v[198:199], off
	v_lshl_add_u64 v[198:199], v[214:215], 0, s[42:43]
	s_mov_b32 m0, s36
	s_nop 0
	global_load_lds_dwordx4 v[198:199], off
	v_lshl_add_u64 v[198:199], v[216:217], 0, s[42:43]
	s_mov_b32 m0, s40
	s_nop 0
	global_load_lds_dwordx4 v[198:199], off
	s_waitcnt vmcnt(8)
	s_cmp_lg_u32 s64, 4
	s_cbranch_scc1 .Lmg_nopf
	s_lshl_b32 s20, s4, 8
	s_lshl_b32 s21, s0, 8
	s_cmp_gt_i32 s0, 3
	s_cbranch_scc1 .Lmg_pf2
	v_add_u32_e32 v253, s20, v200
	v_or_b32_e32 v252, s21, v202
	v_lshl_add_u32 v252, v253, 10, v252
	global_load_dwordx2 v[228:229], v252, s[10:11]
	global_load_dwordx2 v[232:233], v252, s[34:35]
	global_load_dwordx2 v[230:231], v252, s[10:11] offset:128
	global_load_dwordx2 v[234:235], v252, s[34:35] offset:128
	v_add_u32_e32 v252, 0x4000, v252
	global_load_dwordx2 v[236:237], v252, s[10:11]
	global_load_dwordx2 v[240:241], v252, s[34:35]
	global_load_dwordx2 v[238:239], v252, s[10:11] offset:128
	global_load_dwordx2 v[242:243], v252, s[34:35] offset:128
	v_add_u32_e32 v252, 0x4000, v252
	global_load_dwordx2 v[244:245], v252, s[10:11]
	global_load_dwordx2 v[248:249], v252, s[34:35]
	global_load_dwordx2 v[246:247], v252, s[10:11] offset:128
	global_load_dwordx2 v[250:251], v252, s[34:35] offset:128
	s_branch .Lmg_nopf

; __device__ __forceinline__ unsigned xb_ld(unsigned* p)              { return __hip_atomic_load(p, __ATOMIC_RELAXED, __HIP_MEMORY_SCOPE_AGENT); }
; __device__ __forceinline__ unsigned xb_add(unsigned* p, unsigned v) { return __hip_atomic_fetch_add(p, v, __ATOMIC_RELAXED, __HIP_MEMORY_SCOPE_AGENT); }
; #define XB_SPIN(cond, bar) do { unsigned _sp = 0; while (cond) { __builtin_amdgcn_s_sleep(1); \
;     if ((++_sp & 255u) == 0u) { if (xb_ld(&(bar)[XB_TMO])) break; if (_sp > XB_SPIN_CAP) { atomicAdd(&(bar)[XB_TMO], 1u); break; } } } } while (0)
; __device__ __forceinline__ void xcd_barrier(const XcdBarrier& b, const bool group_local = false, const bool xcc_only = false) {
;     ...
;         if (old + 1u == (gen + 1u) * nloc) {
;             const bool fast = group_local && b.st[2] == 2u;
;             if (!fast) {
;             __builtin_amdgcn_fence(__ATOMIC_RELEASE, "agent");
;             asm volatile("s_waitcnt vmcnt(0)" ::: "memory"); }
;             if (!(fast && xcc_only)) {
;             const unsigned og = xb_add(&bar[XB_TOP], 1u);
;             const unsigned tg = og / nx;
;             if (og + 1u == (tg + 1u) * nx) xb_add(&bar[XB_TOPGEN], 1u);
;             else XB_SPIN(xb_ld(&bar[XB_TOPGEN]) == tg, bar);
;             }
;             asm volatile("" ::: "memory");
;             xb_add(&bar[XB_XGEN(b.x)], 1u);
;             __builtin_amdgcn_fence(__ATOMIC_ACQUIRE, "agent");
;             asm volatile("s_waitcnt vmcnt(0)" ::: "memory");
;         } else {
;             XB_SPIN(xb_ld(&bar[XB_XGEN(b.x)]) <= gen, bar);
;     ...
;             __builtin_amdgcn_fence(__ATOMIC_ACQUIRE, "agent");
;     ...
;             asm volatile("s_waitcnt vmcnt(0)" ::: "memory");
;         }
.LBB0_1263:
	s_add_u32 s4, s6, 0x2400
	s_addc_u32 s5, s7, 0
	v_mov_b64_e32 v[4:5], s[4:5]
	s_or_b64 s[12:13], s[12:13], exec
	s_or_b64 exec, exec, s[0:1]
	s_and_saveexec_b64 s[0:1], s[12:13]
	s_cbranch_execnz .LBB0_1106
	s_branch .LBB0_1107
	.p2align 6
	s_nop 0
	s_nop 0
	s_nop 0
	s_nop 0
.LBB0_1264:
	s_or_b64 exec, exec, s[26:27]
	s_and_b64 s[26:27], s[28:29], exec

;     __device__ __forceinline__ void a_ready(const Unit&) const { if (++ncall == 3 && sig != nullptr && threadIdx.x == 0) __hip_atomic_fetch_add(sig, 1u, __ATOMIC_RELAXED, __HIP_MEMORY_SCOPE_AGENT); }
; #define PG8_STAGE(bufoff, gbase, voff) do { _Pragma("unroll") for (int _i = 0; _i < 2; ++_i) \
;         __builtin_amdgcn_global_load_lds((const unsigned*)((const char*)(gbase) + (voff)[_i]), (PG8_LAS unsigned*)(lds + (bufoff) + ldsw + _i * 8192), 16, 0, 0); } while (0)
; #define PG8_LDA(dst, b, h) do { _Pragma("unroll") for (int m = 0; m < 4; ++m) _Pragma("unroll") for (int k = 0; k < 2; ++k) dst[m][k] = *(const PG8_LAS bf16x8*)(lds + PG8_SA(b, h) + aoff + m * 2048 + k * 1024); } while (0)
; #define PG8_BAR __builtin_amdgcn_s_barrier()
; template <class Epi, class Sched, bool ALIGN_EPI = false, bool SP2 = false>
; __device__ __forceinline__ void gemm_phase(PG8_LAS unsigned char* lds, const Gemm g, const Sched& S, const Epi& E) {
;     ...
;         for (int t = 0; t < nt; t += 2) {
;             const bool last = (t == nt - 2);
;             const char* a1 = cA + (size_t)(t + 1) * kstep;
;             const char* a2 = last ? nA : cA + (size_t)(t + 2) * kstep; const char* b2 = last ? nB : cB + (size_t)(t + 2) * kstep;
;             const char* a3 = a2 + kstep; const char* b3 = b2 + kstep;
;             if (last && has_next) S.a_ready(nxt);
;             if constexpr (SP2) {
;             PG8_LDB(B0, 0, 0); PG8_LDB(B1, 0, 1); PG8_SCHED; PG8_LDA(At, 0, 0); PG8_STAGE(PG8_SA(1, 1), a1 + hstep, voffA);
;     ...
;             if (PROBE_KIND == 18 && t == 0 && ui > 0 && g.probe) { const unsigned long long tq_ = __builtin_amdgcn_s_memrealtime(); PG8_WAIT_V(8); pg8_probe_acc += (unsigned)(__builtin_amdgcn_s_memrealtime() - tq_); }
;     ...
;             PG8_WAIT_V(8); PG8_WAIT_L(0); PG8_BAR; PG8_MMA(0, 0, At, B0); PG8_MMA(0, 1, At, B1); PG8_BAR; PG8_SCHED;
;             PG8_LDA(At, 0, 1); PG8_STAGE(PG8_SB(0, 0), b2, voffB); PG8_STAGE(PG8_SB(0, 1), b2 + hstep, voffB); PG8_STAGE(PG8_SA(0, 0), a2, voffA);
;             PG8_WAIT_V(8); PG8_WAIT_L(0); PG8_BAR; if (cur.half == 0) { PG8_MMA(1, 0, At, B0); PG8_MMA(1, 1, At, B1); } PG8_BAR; PG8_SCHED;
;             PG8_LDB(B0, 1, 0); PG8_LDB(B1, 1, 1); PG8_SCHED; PG8_LDA(At, 1, 0); PG8_STAGE(PG8_SA(0, 1), a2 + hstep, voffA);
;             PG8_WAIT_V(8); PG8_WAIT_L(0); PG8_BAR; PG8_MMA(0, 0, At, B0); PG8_MMA(0, 1, At, B1); PG8_BAR; PG8_SCHED;
.LBB0_1300:
	s_add_u32 s28, s4, s0
	s_addc_u32 s29, s5, s1
	s_add_u32 s28, s28, 0x100
	s_addc_u32 s29, s29, 0
	s_add_u32 s67, s62, s0
	s_addc_u32 s68, s63, s1
	s_add_i32 s69, 0, 0x10000
	s_cmpk_eq_i32 s0, 0x700
	s_cselect_b32 s31, s7, s29
	s_cselect_b32 s30, s64, s28
	s_cselect_b32 s29, s11, s68
	s_cselect_b32 s28, s65, s67
	s_add_i32 s67, 0, 0x14000
	v_add_u32_e32 v162, s69, v148
	v_add_u32_e32 v178, s67, v148
	ds_read_b128 v[150:153], v162
	ds_read_b128 v[154:157], v162 offset:1024
	ds_read_b128 v[158:161], v162 offset:2048
	ds_read_b128 v[162:165], v162 offset:3072
	ds_read_b128 v[166:169], v178
	ds_read_b128 v[170:173], v178 offset:1024
	ds_read_b128 v[174:177], v178 offset:2048
	ds_read_b128 v[178:181], v178 offset:3072
	v_lshl_add_u64 v[216:217], v[142:143], 0, s[0:1]
	s_add_i32 m0, s40, 0xc000
	ds_read_b128 v[182:185], v149
	ds_read_b128 v[186:189], v149 offset:1024
	ds_read_b128 v[190:193], v149 offset:2048
	ds_read_b128 v[194:197], v149 offset:3072
	ds_read_b128 v[198:201], v149 offset:4096
	ds_read_b128 v[202:205], v149 offset:5120
	ds_read_b128 v[206:209], v149 offset:6144
	ds_read_b128 v[210:213], v149 offset:7168
	global_load_lds_dwordx4 v[216:217], off
	v_lshl_add_u64 v[216:217], v[144:145], 0, s[0:1]
	s_add_i32 m0, s40, 0xe000
	s_nop 0
	global_load_lds_dwordx4 v[216:217], off
	s_waitcnt vmcnt(8)
	s_waitcnt lgkmcnt(0)
	s_barrier
	s_setprio 1
	s_waitcnt lgkmcnt(0)
	v_mfma_f32_16x16x32_bf16 v[128:131], v[150:153], v[182:185], v[128:131]
	v_mfma_f32_16x16x32_bf16 v[124:127], v[158:161], v[182:185], v[124:127]
	v_mfma_f32_16x16x32_bf16 v[112:115], v[150:153], v[190:193], v[112:115]
	v_mfma_f32_16x16x32_bf16 v[108:111], v[158:161], v[190:193], v[108:111]
	v_mfma_f32_16x16x32_bf16 v[96:99], v[150:153], v[198:201], v[96:99]
	v_mfma_f32_16x16x32_bf16 v[92:95], v[158:161], v[198:201], v[92:95]
	v_mfma_f32_16x16x32_bf16 v[80:83], v[150:153], v[206:209], v[80:83]
	v_mfma_f32_16x16x32_bf16 v[76:79], v[158:161], v[206:209], v[76:79]
	v_mfma_f32_16x16x32_bf16 v[128:131], v[154:157], v[186:189], v[128:131]
	v_mfma_f32_16x16x32_bf16 v[124:127], v[162:165], v[186:189], v[124:127]
	v_mfma_f32_16x16x32_bf16 v[112:115], v[154:157], v[194:197], v[112:115]
	v_mfma_f32_16x16x32_bf16 v[108:111], v[162:165], v[194:197], v[108:111]
	v_mfma_f32_16x16x32_bf16 v[96:99], v[154:157], v[202:205], v[96:99]
	v_mfma_f32_16x16x32_bf16 v[92:95], v[162:165], v[202:205], v[92:95]
	v_mfma_f32_16x16x32_bf16 v[80:83], v[154:157], v[210:213], v[80:83]
	v_mfma_f32_16x16x32_bf16 v[76:79], v[162:165], v[210:213], v[76:79]
	s_setprio 0
	s_setprio 1
	v_mfma_f32_16x16x32_bf16 v[120:123], v[166:169], v[182:185], v[120:123]
	v_mfma_f32_16x16x32_bf16 v[116:119], v[174:177], v[182:185], v[116:119]
	v_mfma_f32_16x16x32_bf16 v[104:107], v[166:169], v[190:193], v[104:107]
	v_mfma_f32_16x16x32_bf16 v[100:103], v[174:177], v[190:193], v[100:103]
	v_mfma_f32_16x16x32_bf16 v[88:91], v[166:169], v[198:201], v[88:91]
	v_mfma_f32_16x16x32_bf16 v[84:87], v[174:177], v[198:201], v[84:87]
	v_mfma_f32_16x16x32_bf16 v[72:75], v[166:169], v[206:209], v[72:75]
	v_mfma_f32_16x16x32_bf16 v[68:71], v[174:177], v[206:209], v[68:71]
	v_mfma_f32_16x16x32_bf16 v[120:123], v[170:173], v[186:189], v[120:123]
	v_mfma_f32_16x16x32_bf16 v[116:119], v[178:181], v[186:189], v[116:119]
	v_mfma_f32_16x16x32_bf16 v[104:107], v[170:173], v[194:197], v[104:107]
	v_mfma_f32_16x16x32_bf16 v[100:103], v[178:181], v[194:197], v[100:103]
	v_mfma_f32_16x16x32_bf16 v[88:91], v[170:173], v[202:205], v[88:91]
	v_mfma_f32_16x16x32_bf16 v[84:87], v[178:181], v[202:205], v[84:87]
	v_mfma_f32_16x16x32_bf16 v[72:75], v[170:173], v[210:213], v[72:75]
	v_mfma_f32_16x16x32_bf16 v[68:71], v[178:181], v[210:213], v[68:71]
	s_setprio 0
	s_barrier
	s_add_i32 s68, s69, s39
	v_lshl_add_u64 v[216:217], s[28:29], 0, v[2:3]
	s_mov_b32 m0, s68
	ds_read_b128 v[182:185], v149 offset:16384
	ds_read_b128 v[186:189], v149 offset:17408
	ds_read_b128 v[190:193], v149 offset:18432
	ds_read_b128 v[194:197], v149 offset:19456
	ds_read_b128 v[198:201], v149 offset:20480
	ds_read_b128 v[202:205], v149 offset:21504
	ds_read_b128 v[206:209], v149 offset:22528
	ds_read_b128 v[210:213], v149 offset:23552
	global_load_lds_dwordx4 v[216:217], off
	s_add_i32 m0, s68, 0x2000
	s_add_u32 s68, s28, 0x40000
	v_lshl_add_u64 v[218:219], s[28:29], 0, v[136:137]
	s_addc_u32 s69, s29, 0
	s_add_i32 s67, s67, s39
	global_load_lds_dwordx4 v[218:219], off
	v_lshl_add_u64 v[220:221], s[68:69], 0, v[2:3]
	s_mov_b32 m0, s67
	v_lshl_add_u64 v[228:229], s[30:31], 0, v[134:135]
	global_load_lds_dwordx4 v[220:221], off
	v_lshl_add_u64 v[220:221], s[68:69], 0, v[136:137]
	s_add_i32 m0, s67, 0x2000
	s_nop 0
	global_load_lds_dwordx4 v[220:221], off
	v_lshl_add_u64 v[220:221], s[30:31], 0, v[132:133]
	s_mov_b32 m0, s40
	s_nop 0
	global_load_lds_dwordx4 v[220:221], off
	s_mov_b32 m0, s41
	s_nop 0
	global_load_lds_dwordx4 v[228:229], off
	s_nop 0
	s_waitcnt vmcnt(8)
	s_waitcnt lgkmcnt(0)
	s_barrier
; #define PG8_STAGE(bufoff, gbase, voff) do { _Pragma("unroll") for (int _i = 0; _i < 2; ++_i) \
;         __builtin_amdgcn_global_load_lds((const unsigned*)((const char*)(gbase) + (voff)[_i]), (PG8_LAS unsigned*)(lds + (bufoff) + ldsw + _i * 8192), 16, 0, 0); } while (0)
; #define PG8_LDA(dst, b, h) do { _Pragma("unroll") for (int m = 0; m < 4; ++m) _Pragma("unroll") for (int k = 0; k < 2; ++k) dst[m][k] = *(const PG8_LAS bf16x8*)(lds + PG8_SA(b, h) + aoff + m * 2048 + k * 1024); } while (0)
; #define PG8_LDB(dst, b, h) do { _Pragma("unroll") for (int n = 0; n < 2; ++n) _Pragma("unroll") for (int k = 0; k < 2; ++k) dst[n][k] = *(const PG8_LAS bf16x8*)(lds + PG8_SB(b, h) + boff + n * 2048 + k * 1024); } while (0)
; #define PG8_MMA(ai, bj, At, Bt) do { __builtin_amdgcn_s_setprio(1); _Pragma("unroll") for (int m = 0; m < 4; ++m) _Pragma("unroll") for (int n = 0; n < 2; ++n) _Pragma("unroll") for (int k = 0; k < 2; ++k) \
;         acc[ai][bj][m][n] = __builtin_amdgcn_mfma_f32_16x16x32_bf16(Bt[n][k], At[m][k], acc[ai][bj][m][n], 0, 0, 0); __builtin_amdgcn_s_setprio(0); } while (0)
; #define PG8_WAIT_V(n) asm volatile("s_waitcnt vmcnt(" #n ")" ::: "memory")
; #define PG8_WAIT_L(n) asm volatile("s_waitcnt lgkmcnt(" #n ")" ::: "memory")
; #define PG8_BAR __builtin_amdgcn_s_barrier()
; #define PG8_SCHED __builtin_amdgcn_sched_barrier(0)
; template <class Epi, class Sched, bool ALIGN_EPI = false, bool SP2 = false>
; __device__ __forceinline__ void gemm_phase(PG8_LAS unsigned char* lds, const Gemm g, const Sched& S, const Epi& E) {
;     ...
;             PG8_WAIT_V(8); PG8_WAIT_L(0); PG8_BAR; if (cur.half == 0) { PG8_MMA(1, 0, At, B0); PG8_MMA(1, 1, At, B1); } PG8_BAR; PG8_SCHED;
;             PG8_LDB(B0, 1, 0); PG8_LDB(B1, 1, 1); PG8_SCHED; PG8_LDA(At, 1, 0); PG8_STAGE(PG8_SA(0, 1), a2 + hstep, voffA);
;             PG8_WAIT_V(8); PG8_WAIT_L(0); PG8_BAR; PG8_MMA(0, 0, At, B0); PG8_MMA(0, 1, At, B1); PG8_BAR; PG8_SCHED;
;             PG8_LDA(At, 1, 1); PG8_STAGE(PG8_SB(1, 0), b3, voffB); PG8_STAGE(PG8_SB(1, 1), b3 + hstep, voffB); PG8_STAGE(PG8_SA(1, 0), a3, voffA);
;             PG8_WAIT_V(8); PG8_WAIT_L(0); PG8_BAR; if (cur.half == 0) { PG8_MMA(1, 0, At, B0); PG8_MMA(1, 1, At, B1); } PG8_BAR; PG8_SCHED;
	s_setprio 1
	s_waitcnt lgkmcnt(0)
	v_mfma_f32_16x16x32_bf16 v[64:67], v[150:153], v[182:185], v[64:67]
	v_mfma_f32_16x16x32_bf16 v[60:63], v[158:161], v[182:185], v[60:63]
	v_mfma_f32_16x16x32_bf16 v[48:51], v[150:153], v[190:193], v[48:51]
	v_mfma_f32_16x16x32_bf16 v[44:47], v[158:161], v[190:193], v[44:47]
	v_mfma_f32_16x16x32_bf16 v[32:35], v[150:153], v[198:201], v[32:35]
	v_mfma_f32_16x16x32_bf16 v[28:31], v[158:161], v[198:201], v[28:31]
	v_mfma_f32_16x16x32_bf16 v[16:19], v[150:153], v[206:209], v[16:19]
	v_mfma_f32_16x16x32_bf16 v[12:15], v[158:161], v[206:209], v[12:15]
	v_mfma_f32_16x16x32_bf16 v[64:67], v[154:157], v[186:189], v[64:67]
	v_mfma_f32_16x16x32_bf16 v[60:63], v[162:165], v[186:189], v[60:63]
	v_mfma_f32_16x16x32_bf16 v[48:51], v[154:157], v[194:197], v[48:51]
	v_mfma_f32_16x16x32_bf16 v[44:47], v[162:165], v[194:197], v[44:47]
	v_mfma_f32_16x16x32_bf16 v[32:35], v[154:157], v[202:205], v[32:35]
	v_mfma_f32_16x16x32_bf16 v[28:31], v[162:165], v[202:205], v[28:31]
	v_mfma_f32_16x16x32_bf16 v[16:19], v[154:157], v[210:213], v[16:19]
	v_mfma_f32_16x16x32_bf16 v[12:15], v[162:165], v[210:213], v[12:15]
	s_setprio 0
	s_setprio 1
	v_mfma_f32_16x16x32_bf16 v[56:59], v[166:169], v[182:185], v[56:59]
	v_mfma_f32_16x16x32_bf16 v[52:55], v[174:177], v[182:185], v[52:55]
	v_mfma_f32_16x16x32_bf16 v[40:43], v[166:169], v[190:193], v[40:43]
	v_mfma_f32_16x16x32_bf16 v[36:39], v[174:177], v[190:193], v[36:39]
	v_mfma_f32_16x16x32_bf16 v[24:27], v[166:169], v[198:201], v[24:27]
	v_mfma_f32_16x16x32_bf16 v[20:23], v[174:177], v[198:201], v[20:23]
	v_mfma_f32_16x16x32_bf16 v[8:11], v[166:169], v[206:209], v[8:11]
	v_mfma_f32_16x16x32_bf16 v[4:7], v[174:177], v[206:209], v[4:7]
	v_mfma_f32_16x16x32_bf16 v[56:59], v[170:173], v[186:189], v[56:59]
	v_mfma_f32_16x16x32_bf16 v[52:55], v[178:181], v[186:189], v[52:55]
	v_mfma_f32_16x16x32_bf16 v[40:43], v[170:173], v[194:197], v[40:43]
	v_mfma_f32_16x16x32_bf16 v[36:39], v[178:181], v[194:197], v[36:39]
	v_mfma_f32_16x16x32_bf16 v[24:27], v[170:173], v[202:205], v[24:27]
	v_mfma_f32_16x16x32_bf16 v[20:23], v[178:181], v[202:205], v[20:23]
	v_mfma_f32_16x16x32_bf16 v[8:11], v[170:173], v[210:213], v[8:11]
	v_mfma_f32_16x16x32_bf16 v[4:7], v[178:181], v[210:213], v[4:7]
	s_setprio 0
	s_barrier
	s_add_i32 s67, 0, 0x18000
	s_add_i32 s68, 0, 0x1c000
	v_add_u32_e32 v162, s67, v148
	v_add_u32_e32 v178, s68, v148
	ds_read_b128 v[150:153], v162
	ds_read_b128 v[154:157], v162 offset:1024
	ds_read_b128 v[158:161], v162 offset:2048
	ds_read_b128 v[162:165], v162 offset:3072
	ds_read_b128 v[166:169], v178
	ds_read_b128 v[170:173], v178 offset:1024
	ds_read_b128 v[174:177], v178 offset:2048
	ds_read_b128 v[178:181], v178 offset:3072
	s_add_u32 s30, s30, 0x40000
	s_addc_u32 s31, s31, 0
	s_mov_b32 m0, s56
	v_lshl_add_u64 v[230:231], s[30:31], 0, v[132:133]
	ds_read_b128 v[182:185], v149 offset:32768
	ds_read_b128 v[186:189], v149 offset:33792
	ds_read_b128 v[190:193], v149 offset:34816
	ds_read_b128 v[194:197], v149 offset:35840
	ds_read_b128 v[198:201], v149 offset:36864
	ds_read_b128 v[202:205], v149 offset:37888
	ds_read_b128 v[206:209], v149 offset:38912
	ds_read_b128 v[210:213], v149 offset:39936
	global_load_lds_dwordx4 v[230:231], off
	v_lshl_add_u64 v[230:231], s[30:31], 0, v[134:135]
	s_mov_b32 m0, s57
	s_nop 0
	global_load_lds_dwordx4 v[230:231], off
	s_nop 0
	s_waitcnt vmcnt(8)
	s_waitcnt lgkmcnt(0)
	s_barrier
	s_setprio 1
	s_waitcnt lgkmcnt(0)
	v_mfma_f32_16x16x32_bf16 v[128:131], v[150:153], v[182:185], v[128:131]
	v_mfma_f32_16x16x32_bf16 v[124:127], v[158:161], v[182:185], v[124:127]
	v_mfma_f32_16x16x32_bf16 v[112:115], v[150:153], v[190:193], v[112:115]
	v_mfma_f32_16x16x32_bf16 v[108:111], v[158:161], v[190:193], v[108:111]
	v_mfma_f32_16x16x32_bf16 v[96:99], v[150:153], v[198:201], v[96:99]
	v_mfma_f32_16x16x32_bf16 v[92:95], v[158:161], v[198:201], v[92:95]
	v_mfma_f32_16x16x32_bf16 v[80:83], v[150:153], v[206:209], v[80:83]
	v_mfma_f32_16x16x32_bf16 v[76:79], v[158:161], v[206:209], v[76:79]
	v_mfma_f32_16x16x32_bf16 v[128:131], v[154:157], v[186:189], v[128:131]
	v_mfma_f32_16x16x32_bf16 v[124:127], v[162:165], v[186:189], v[124:127]
	v_mfma_f32_16x16x32_bf16 v[112:115], v[154:157], v[194:197], v[112:115]
	v_mfma_f32_16x16x32_bf16 v[108:111], v[162:165], v[194:197], v[108:111]
	v_mfma_f32_16x16x32_bf16 v[96:99], v[154:157], v[202:205], v[96:99]
	v_mfma_f32_16x16x32_bf16 v[92:95], v[162:165], v[202:205], v[92:95]
	v_mfma_f32_16x16x32_bf16 v[80:83], v[154:157], v[210:213], v[80:83]
	v_mfma_f32_16x16x32_bf16 v[76:79], v[162:165], v[210:213], v[76:79]
	s_setprio 0
	s_setprio 1
	v_mfma_f32_16x16x32_bf16 v[120:123], v[166:169], v[182:185], v[120:123]
	v_mfma_f32_16x16x32_bf16 v[116:119], v[174:177], v[182:185], v[116:119]
	v_mfma_f32_16x16x32_bf16 v[104:107], v[166:169], v[190:193], v[104:107]
	v_mfma_f32_16x16x32_bf16 v[100:103], v[174:177], v[190:193], v[100:103]
	v_mfma_f32_16x16x32_bf16 v[88:91], v[166:169], v[198:201], v[88:91]
	v_mfma_f32_16x16x32_bf16 v[84:87], v[174:177], v[198:201], v[84:87]
	v_mfma_f32_16x16x32_bf16 v[72:75], v[166:169], v[206:209], v[72:75]
	v_mfma_f32_16x16x32_bf16 v[68:71], v[174:177], v[206:209], v[68:71]
	v_mfma_f32_16x16x32_bf16 v[120:123], v[170:173], v[186:189], v[120:123]
	v_mfma_f32_16x16x32_bf16 v[116:119], v[178:181], v[186:189], v[116:119]
	v_mfma_f32_16x16x32_bf16 v[104:107], v[170:173], v[194:197], v[104:107]
	v_mfma_f32_16x16x32_bf16 v[100:103], v[178:181], v[194:197], v[100:103]
	v_mfma_f32_16x16x32_bf16 v[88:91], v[170:173], v[202:205], v[88:91]
	v_mfma_f32_16x16x32_bf16 v[84:87], v[178:181], v[202:205], v[84:87]
	v_mfma_f32_16x16x32_bf16 v[72:75], v[170:173], v[210:213], v[72:75]
	v_mfma_f32_16x16x32_bf16 v[68:71], v[178:181], v[210:213], v[68:71]
	s_setprio 0
	s_barrier
; template <class Epi, class Sched, bool ALIGN_EPI = false, bool SP2 = false>
; __device__ __forceinline__ void gemm_phase(PG8_LAS unsigned char* lds, const Gemm g, const Sched& S, const Epi& E) {
;     ...
;         if (!has_next) break;
;         if constexpr (!Epi::CHAIN) {
; #pragma unroll
;         for (int a = 0; a < 2; ++a)
; #pragma unroll
;             for (int b = 0; b < 2; ++b)
; #pragma unroll
;                 for (int m = 0; m < 4; ++m)
; #pragma unroll
;                     for (int n = 0; n < 2; ++n) acc[a][b][m][n] = (f32x4){0.f, 0.f, 0.f, 0.f};
;         }
;         cur = nxt; cA = nA; cB = nB; ++ui;
	s_add_i32 s30, s67, s39
	v_lshl_add_u64 v[216:217], v[216:217], 0, s[42:43]
	s_mov_b32 m0, s30
	ds_read_b128 v[182:185], v149 offset:49152
	ds_read_b128 v[186:189], v149 offset:50176
	ds_read_b128 v[190:193], v149 offset:51200
	ds_read_b128 v[194:197], v149 offset:52224
	ds_read_b128 v[198:201], v149 offset:53248
	ds_read_b128 v[202:205], v149 offset:54272
	ds_read_b128 v[206:209], v149 offset:55296
	ds_read_b128 v[210:213], v149 offset:56320
	global_load_lds_dwordx4 v[216:217], off
	s_add_i32 m0, s30, 0x2000
	s_add_u32 s28, s28, 0x40080
	v_lshl_add_u64 v[216:217], v[218:219], 0, s[42:43]
	s_addc_u32 s29, s29, 0
	s_add_i32 s30, s68, s39
	global_load_lds_dwordx4 v[216:217], off
	v_lshl_add_u64 v[216:217], s[28:29], 0, v[2:3]
	s_mov_b32 m0, s30
	s_nop 0
	global_load_lds_dwordx4 v[216:217], off
	v_lshl_add_u64 v[216:217], s[28:29], 0, v[136:137]
	s_add_i32 m0, s30, 0x2000
	s_nop 0
	global_load_lds_dwordx4 v[216:217], off
	v_lshl_add_u64 v[216:217], v[220:221], 0, s[42:43]
	s_mov_b32 m0, s58
	s_nop 0
	global_load_lds_dwordx4 v[216:217], off
	v_lshl_add_u64 v[216:217], v[228:229], 0, s[42:43]
	s_mov_b32 m0, s59
	s_nop 0
	global_load_lds_dwordx4 v[216:217], off
	s_waitcnt vmcnt(8)
	s_waitcnt lgkmcnt(0)
	s_barrier
	s_setprio 1
	s_waitcnt lgkmcnt(0)
	v_mfma_f32_16x16x32_bf16 v[64:67], v[150:153], v[182:185], v[64:67]
	v_mfma_f32_16x16x32_bf16 v[60:63], v[158:161], v[182:185], v[60:63]
	v_mfma_f32_16x16x32_bf16 v[48:51], v[150:153], v[190:193], v[48:51]
	v_mfma_f32_16x16x32_bf16 v[44:47], v[158:161], v[190:193], v[44:47]
	v_mfma_f32_16x16x32_bf16 v[32:35], v[150:153], v[198:201], v[32:35]
	v_mfma_f32_16x16x32_bf16 v[28:31], v[158:161], v[198:201], v[28:31]
	v_mfma_f32_16x16x32_bf16 v[16:19], v[150:153], v[206:209], v[16:19]
	v_mfma_f32_16x16x32_bf16 v[12:15], v[158:161], v[206:209], v[12:15]
	v_mfma_f32_16x16x32_bf16 v[64:67], v[154:157], v[186:189], v[64:67]
	v_mfma_f32_16x16x32_bf16 v[60:63], v[162:165], v[186:189], v[60:63]
	v_mfma_f32_16x16x32_bf16 v[48:51], v[154:157], v[194:197], v[48:51]
	v_mfma_f32_16x16x32_bf16 v[44:47], v[162:165], v[194:197], v[44:47]
	v_mfma_f32_16x16x32_bf16 v[32:35], v[154:157], v[202:205], v[32:35]
	v_mfma_f32_16x16x32_bf16 v[28:31], v[162:165], v[202:205], v[28:31]
	v_mfma_f32_16x16x32_bf16 v[16:19], v[154:157], v[210:213], v[16:19]
	v_mfma_f32_16x16x32_bf16 v[12:15], v[162:165], v[210:213], v[12:15]
	s_setprio 0
	s_setprio 1
	v_mfma_f32_16x16x32_bf16 v[56:59], v[166:169], v[182:185], v[56:59]
	v_mfma_f32_16x16x32_bf16 v[52:55], v[174:177], v[182:185], v[52:55]
	v_mfma_f32_16x16x32_bf16 v[40:43], v[166:169], v[190:193], v[40:43]
	v_mfma_f32_16x16x32_bf16 v[36:39], v[174:177], v[190:193], v[36:39]
	v_mfma_f32_16x16x32_bf16 v[24:27], v[166:169], v[198:201], v[24:27]
	v_mfma_f32_16x16x32_bf16 v[20:23], v[174:177], v[198:201], v[20:23]
	v_mfma_f32_16x16x32_bf16 v[8:11], v[166:169], v[206:209], v[8:11]
	v_mfma_f32_16x16x32_bf16 v[4:7], v[174:177], v[206:209], v[4:7]
	v_mfma_f32_16x16x32_bf16 v[56:59], v[170:173], v[186:189], v[56:59]
	v_mfma_f32_16x16x32_bf16 v[52:55], v[178:181], v[186:189], v[52:55]
	v_mfma_f32_16x16x32_bf16 v[40:43], v[170:173], v[194:197], v[40:43]
	v_mfma_f32_16x16x32_bf16 v[36:39], v[178:181], v[194:197], v[36:39]
	v_mfma_f32_16x16x32_bf16 v[24:27], v[170:173], v[202:205], v[24:27]
	v_mfma_f32_16x16x32_bf16 v[20:23], v[178:181], v[202:205], v[20:23]
	v_mfma_f32_16x16x32_bf16 v[8:11], v[170:173], v[210:213], v[8:11]
	v_mfma_f32_16x16x32_bf16 v[4:7], v[178:181], v[210:213], v[4:7]
	s_setprio 0
	s_barrier
	s_add_i32 s66, s66, 2
	s_add_u32 s0, s0, 0x100
	s_addc_u32 s1, s1, 0
	s_cmp_gt_u32 s66, 13
	s_cbranch_scc0 .LBB0_1300
	s_add_u32 s0, s62, 0xffffff00
	s_addc_u32 s1, s63, -1
	s_andn2_b64 vcc, exec, s[20:21]
	s_cbranch_vccnz .LBB0_1303
	v_mov_b32_e32 v4, 0
	s_mov_b32 s16, s10
	s_mov_b32 s8, s6
	s_mov_b64 s[4:5], s[26:27]
	s_mov_b32 s60, s61
	v_mov_b32_e32 v5, v4
	v_mov_b32_e32 v6, v4
	v_mov_b32_e32 v7, v4
	v_mov_b32_e32 v8, v4
	v_mov_b32_e32 v9, v4
	v_mov_b32_e32 v10, v4
	v_mov_b32_e32 v11, v4
	v_mov_b32_e32 v20, v4
	v_mov_b32_e32 v21, v4
	v_mov_b32_e32 v22, v4
	v_mov_b32_e32 v23, v4
	v_mov_b32_e32 v24, v4
	v_mov_b32_e32 v25, v4
	v_mov_b32_e32 v26, v4
	v_mov_b32_e32 v27, v4
	v_mov_b32_e32 v36, v4
	v_mov_b32_e32 v37, v4
	v_mov_b32_e32 v38, v4
	v_mov_b32_e32 v39, v4
	v_mov_b32_e32 v40, v4
	v_mov_b32_e32 v41, v4
	v_mov_b32_e32 v42, v4
	v_mov_b32_e32 v43, v4
	v_mov_b32_e32 v52, v4
	v_mov_b32_e32 v53, v4
	v_mov_b32_e32 v54, v4
	v_mov_b32_e32 v55, v4
	v_mov_b32_e32 v56, v4
	v_mov_b32_e32 v57, v4
	v_mov_b32_e32 v58, v4
	v_mov_b32_e32 v59, v4
	v_mov_b32_e32 v12, v4
	v_mov_b32_e32 v13, v4
	v_mov_b32_e32 v14, v4
	v_mov_b32_e32 v15, v4
	v_mov_b32_e32 v16, v4
	v_mov_b32_e32 v17, v4
	v_mov_b32_e32 v18, v4
	v_mov_b32_e32 v19, v4
	v_mov_b32_e32 v28, v4
	v_mov_b32_e32 v29, v4
	v_mov_b32_e32 v30, v4
	v_mov_b32_e32 v31, v4
	v_mov_b32_e32 v32, v4
	v_mov_b32_e32 v33, v4
	v_mov_b32_e32 v34, v4
	v_mov_b32_e32 v35, v4
	v_mov_b32_e32 v44, v4
	v_mov_b32_e32 v45, v4
	v_mov_b32_e32 v46, v4
	v_mov_b32_e32 v47, v4
	v_mov_b32_e32 v48, v4
	v_mov_b32_e32 v49, v4
	v_mov_b32_e32 v50, v4
	v_mov_b32_e32 v51, v4
	v_mov_b32_e32 v60, v4
	v_mov_b32_e32 v61, v4
	v_mov_b32_e32 v62, v4
	v_mov_b32_e32 v63, v4
	v_mov_b32_e32 v64, v4
	v_mov_b32_e32 v65, v4
	v_mov_b32_e32 v66, v4
	v_mov_b32_e32 v67, v4
	v_mov_b32_e32 v68, v4
	v_mov_b32_e32 v69, v4
	v_mov_b32_e32 v70, v4
	v_mov_b32_e32 v71, v4
	v_mov_b32_e32 v72, v4
	v_mov_b32_e32 v73, v4
	v_mov_b32_e32 v74, v4
	v_mov_b32_e32 v75, v4
	v_mov_b32_e32 v84, v4
	v_mov_b32_e32 v85, v4
	v_mov_b32_e32 v86, v4
	v_mov_b32_e32 v87, v4
	v_mov_b32_e32 v88, v4
	v_mov_b32_e32 v89, v4
	v_mov_b32_e32 v90, v4
	v_mov_b32_e32 v91, v4
	v_mov_b32_e32 v100, v4
	v_mov_b32_e32 v101, v4
	v_mov_b32_e32 v102, v4
	v_mov_b32_e32 v103, v4
	v_mov_b32_e32 v104, v4
	v_mov_b32_e32 v105, v4
	v_mov_b32_e32 v106, v4
	v_mov_b32_e32 v107, v4
	v_mov_b32_e32 v116, v4
	v_mov_b32_e32 v117, v4
	v_mov_b32_e32 v118, v4
	v_mov_b32_e32 v119, v4
	v_mov_b32_e32 v120, v4
	v_mov_b32_e32 v121, v4
	v_mov_b32_e32 v122, v4
	v_mov_b32_e32 v123, v4
	v_mov_b32_e32 v76, v4
	v_mov_b32_e32 v77, v4
	v_mov_b32_e32 v78, v4
	v_mov_b32_e32 v79, v4
	v_mov_b32_e32 v80, v4
	v_mov_b32_e32 v81, v4
	v_mov_b32_e32 v82, v4
	v_mov_b32_e32 v83, v4
	v_mov_b32_e32 v92, v4
	v_mov_b32_e32 v93, v4
	v_mov_b32_e32 v94, v4
	v_mov_b32_e32 v95, v4
	v_mov_b32_e32 v96, v4
	v_mov_b32_e32 v97, v4
	v_mov_b32_e32 v98, v4
	v_mov_b32_e32 v99, v4
	v_mov_b32_e32 v108, v4
	v_mov_b32_e32 v109, v4
	v_mov_b32_e32 v110, v4
	v_mov_b32_e32 v111, v4
	v_mov_b32_e32 v112, v4
	v_mov_b32_e32 v113, v4
	v_mov_b32_e32 v114, v4
	v_mov_b32_e32 v115, v4
	v_mov_b32_e32 v124, v4
	v_mov_b32_e32 v125, v4
	v_mov_b32_e32 v126, v4
	v_mov_b32_e32 v127, v4
	v_mov_b32_e32 v128, v4
	v_mov_b32_e32 v129, v4
	v_mov_b32_e32 v130, v4
	v_mov_b32_e32 v131, v4
	s_andn2_b64 vcc, exec, s[14:15]
	s_cbranch_vccnz .LBB0_1304
	s_branch .LBB0_1305

; #define PG8_STAGE(bufoff, gbase, voff) do { _Pragma("unroll") for (int _i = 0; _i < 2; ++_i) \
;         __builtin_amdgcn_global_load_lds((const unsigned*)((const char*)(gbase) + (voff)[_i]), (PG8_LAS unsigned*)(lds + (bufoff) + ldsw + _i * 8192), 16, 0, 0); } while (0)
; #define PG8_LDA(dst, b, h) do { _Pragma("unroll") for (int m = 0; m < 4; ++m) _Pragma("unroll") for (int k = 0; k < 2; ++k) dst[m][k] = *(const PG8_LAS bf16x8*)(lds + PG8_SA(b, h) + aoff + m * 2048 + k * 1024); } while (0)
; #define PG8_LDB(dst, b, h) do { _Pragma("unroll") for (int n = 0; n < 2; ++n) _Pragma("unroll") for (int k = 0; k < 2; ++k) dst[n][k] = *(const PG8_LAS bf16x8*)(lds + PG8_SB(b, h) + boff + n * 2048 + k * 1024); } while (0)
; #define PG8_MMA(ai, bj, At, Bt) do { __builtin_amdgcn_s_setprio(1); _Pragma("unroll") for (int m = 0; m < 4; ++m) _Pragma("unroll") for (int n = 0; n < 2; ++n) _Pragma("unroll") for (int k = 0; k < 2; ++k) \
;         acc[ai][bj][m][n] = __builtin_amdgcn_mfma_f32_16x16x32_bf16(Bt[n][k], At[m][k], acc[ai][bj][m][n], 0, 0, 0); __builtin_amdgcn_s_setprio(0); } while (0)
; #define PG8_WAIT_V(n) asm volatile("s_waitcnt vmcnt(" #n ")" ::: "memory")
; #define PG8_WAIT_L(n) asm volatile("s_waitcnt lgkmcnt(" #n ")" ::: "memory")
; #define PG8_BAR __builtin_amdgcn_s_barrier()
; #define PG8_SCHED __builtin_amdgcn_sched_barrier(0)
; template <class Epi, class Sched, bool ALIGN_EPI = false, bool SP2 = false>
; __device__ __forceinline__ void gemm_phase(PG8_LAS unsigned char* lds, const Gemm g, const Sched& S, const Epi& E) {
;     ...
;             PG8_LDB(B0, 0, 0); PG8_LDB(B1, 0, 1); PG8_SCHED; PG8_LDA(At, 0, 0); PG8_STAGE(PG8_SA(1, 1), a1 + hstep, voffA);
;     ...
;             if (PROBE_KIND == 18 && t == 0 && ui > 0 && g.probe) { const unsigned long long tq_ = __builtin_amdgcn_s_memrealtime(); PG8_WAIT_V(8); pg8_probe_acc += (unsigned)(__builtin_amdgcn_s_memrealtime() - tq_); }
;     ...
;             PG8_WAIT_V(8); PG8_WAIT_L(0); PG8_BAR; PG8_MMA(0, 0, At, B0); PG8_MMA(0, 1, At, B1); PG8_BAR; PG8_SCHED;
;             PG8_LDA(At, 0, 1); PG8_STAGE(PG8_SB(0, 0), b2, voffB); PG8_STAGE(PG8_SB(0, 1), b2 + hstep, voffB); PG8_STAGE(PG8_SA(0, 0), a2, voffA);
;             PG8_WAIT_V(8); PG8_WAIT_L(0); PG8_BAR; if (cur.half == 0) { PG8_MMA(1, 0, At, B0); PG8_MMA(1, 1, At, B1); } PG8_BAR; PG8_SCHED;
.Lpj_gu_1:
	s_waitcnt lgkmcnt(0)
	s_barrier
	s_setprio 1
	s_waitcnt lgkmcnt(0)
	v_mfma_f32_16x16x32_bf16 v[128:131], v[142:145], v[180:183], 0
	v_mfma_f32_16x16x32_bf16 v[124:127], v[156:159], v[180:183], 0
	v_mfma_f32_16x16x32_bf16 v[112:115], v[142:145], v[188:191], 0
	v_mfma_f32_16x16x32_bf16 v[108:111], v[156:159], v[188:191], 0
	v_mfma_f32_16x16x32_bf16 v[96:99], v[142:145], v[196:199], 0
	v_mfma_f32_16x16x32_bf16 v[92:95], v[156:159], v[196:199], 0
	v_mfma_f32_16x16x32_bf16 v[80:83], v[142:145], v[204:207], 0
	v_mfma_f32_16x16x32_bf16 v[76:79], v[156:159], v[204:207], 0
	v_mfma_f32_16x16x32_bf16 v[128:131], v[152:155], v[184:187], v[128:131]
	v_mfma_f32_16x16x32_bf16 v[124:127], v[160:163], v[184:187], v[124:127]
	v_mfma_f32_16x16x32_bf16 v[112:115], v[152:155], v[192:195], v[112:115]
	v_mfma_f32_16x16x32_bf16 v[108:111], v[160:163], v[192:195], v[108:111]
	v_mfma_f32_16x16x32_bf16 v[96:99], v[152:155], v[200:203], v[96:99]
	v_mfma_f32_16x16x32_bf16 v[92:95], v[160:163], v[200:203], v[92:95]
	v_mfma_f32_16x16x32_bf16 v[80:83], v[152:155], v[208:211], v[80:83]
	v_mfma_f32_16x16x32_bf16 v[76:79], v[160:163], v[208:211], v[76:79]
	s_setprio 0
	s_setprio 1
	v_mfma_f32_16x16x32_bf16 v[120:123], v[164:167], v[180:183], 0
	v_mfma_f32_16x16x32_bf16 v[116:119], v[172:175], v[180:183], 0
	v_mfma_f32_16x16x32_bf16 v[104:107], v[164:167], v[188:191], 0
	v_mfma_f32_16x16x32_bf16 v[100:103], v[172:175], v[188:191], 0
	v_mfma_f32_16x16x32_bf16 v[88:91], v[164:167], v[196:199], 0
	v_mfma_f32_16x16x32_bf16 v[84:87], v[172:175], v[196:199], 0
	v_mfma_f32_16x16x32_bf16 v[72:75], v[164:167], v[204:207], 0
	v_mfma_f32_16x16x32_bf16 v[68:71], v[172:175], v[204:207], 0
	v_mfma_f32_16x16x32_bf16 v[120:123], v[168:171], v[184:187], v[120:123]
	v_mfma_f32_16x16x32_bf16 v[116:119], v[176:179], v[184:187], v[116:119]
	v_mfma_f32_16x16x32_bf16 v[104:107], v[168:171], v[192:195], v[104:107]
	v_mfma_f32_16x16x32_bf16 v[100:103], v[176:179], v[192:195], v[100:103]
	v_mfma_f32_16x16x32_bf16 v[88:91], v[168:171], v[200:203], v[88:91]
	v_mfma_f32_16x16x32_bf16 v[84:87], v[176:179], v[200:203], v[84:87]
	v_mfma_f32_16x16x32_bf16 v[72:75], v[168:171], v[208:211], v[72:75]
	v_mfma_f32_16x16x32_bf16 v[68:71], v[176:179], v[208:211], v[68:71]
	s_setprio 0
	s_barrier
	s_add_i32 s67, s67, s25
	v_lshl_add_u64 v[212:213], s[0:1], 0, v[2:3]
	s_mov_b32 m0, s67
	ds_read_b128 v[180:183], v150 offset:16384
	ds_read_b128 v[184:187], v150 offset:17408
	ds_read_b128 v[188:191], v150 offset:18432
	ds_read_b128 v[192:195], v150 offset:19456
	ds_read_b128 v[196:199], v150 offset:20480
	ds_read_b128 v[200:203], v150 offset:21504
	ds_read_b128 v[204:207], v150 offset:22528
	ds_read_b128 v[208:211], v150 offset:23552
	global_load_lds_dwordx4 v[212:213], off
	s_add_i32 m0, s67, 0x2000
	s_add_u32 s68, s0, 0x40000
	v_lshl_add_u64 v[214:215], s[0:1], 0, v[136:137]
	s_addc_u32 s69, s1, 0
	s_add_i32 s67, s70, s25
	global_load_lds_dwordx4 v[214:215], off
	v_lshl_add_u64 v[216:217], s[68:69], 0, v[2:3]
	s_mov_b32 m0, s67
	v_lshl_add_u64 v[218:219], s[28:29], 0, v[134:135]
	global_load_lds_dwordx4 v[216:217], off
	v_lshl_add_u64 v[216:217], s[68:69], 0, v[136:137]
	s_add_i32 m0, s67, 0x2000
	s_nop 0
	global_load_lds_dwordx4 v[216:217], off
	v_lshl_add_u64 v[216:217], s[28:29], 0, v[132:133]
	s_mov_b32 m0, s15
	s_nop 0
	global_load_lds_dwordx4 v[216:217], off
	s_mov_b32 m0, s21
	s_nop 0
	global_load_lds_dwordx4 v[218:219], off
	s_cmp_eq_u32 s32, 0
	s_cbranch_scc1 .Lpw_gu_2
	s_waitcnt vmcnt(16)
	s_branch .Lpj_gu_2
	.p2align 6
	s_nop 0
	s_nop 0
	s_nop 0
	s_nop 0
	s_nop 0
	s_nop 0
	s_nop 0
	s_nop 0
	s_nop 0
.Lpw_gu_2:
	s_waitcnt vmcnt(8)

;     __device__ __forceinline__ void a_ready(const Unit&) const { if (++ncall == 3 && sig != nullptr && threadIdx.x == 0) __hip_atomic_fetch_add(sig, 1u, __ATOMIC_RELAXED, __HIP_MEMORY_SCOPE_AGENT); }
; #define PG8_STAGE(bufoff, gbase, voff) do { _Pragma("unroll") for (int _i = 0; _i < 2; ++_i) \
;         __builtin_amdgcn_global_load_lds((const unsigned*)((const char*)(gbase) + (voff)[_i]), (PG8_LAS unsigned*)(lds + (bufoff) + ldsw + _i * 8192), 16, 0, 0); } while (0)
; #define PG8_LDA(dst, b, h) do { _Pragma("unroll") for (int m = 0; m < 4; ++m) _Pragma("unroll") for (int k = 0; k < 2; ++k) dst[m][k] = *(const PG8_LAS bf16x8*)(lds + PG8_SA(b, h) + aoff + m * 2048 + k * 1024); } while (0)
; #define PG8_BAR __builtin_amdgcn_s_barrier()
; template <class Epi, class Sched, bool ALIGN_EPI = false, bool SP2 = false>
; __device__ __forceinline__ void gemm_phase(PG8_LAS unsigned char* lds, const Gemm g, const Sched& S, const Epi& E) {
;     ...
;         for (int t = 0; t < nt; t += 2) {
;             const bool last = (t == nt - 2);
;             const char* a1 = cA + (size_t)(t + 1) * kstep;
;             const char* a2 = last ? nA : cA + (size_t)(t + 2) * kstep; const char* b2 = last ? nB : cB + (size_t)(t + 2) * kstep;
;             const char* a3 = a2 + kstep; const char* b3 = b2 + kstep;
;             if (last && has_next) S.a_ready(nxt);
;             if constexpr (SP2) {
;             PG8_LDB(B0, 0, 0); PG8_LDB(B1, 0, 1); PG8_SCHED; PG8_LDA(At, 0, 0); PG8_STAGE(PG8_SA(1, 1), a1 + hstep, voffA);
;     ...
;             if (PROBE_KIND == 18 && t == 0 && ui > 0 && g.probe) { const unsigned long long tq_ = __builtin_amdgcn_s_memrealtime(); PG8_WAIT_V(8); pg8_probe_acc += (unsigned)(__builtin_amdgcn_s_memrealtime() - tq_); }
;     ...
;             PG8_WAIT_V(8); PG8_WAIT_L(0); PG8_BAR; PG8_MMA(0, 0, At, B0); PG8_MMA(0, 1, At, B1); PG8_BAR; PG8_SCHED;
;             PG8_LDA(At, 0, 1); PG8_STAGE(PG8_SB(0, 0), b2, voffB); PG8_STAGE(PG8_SB(0, 1), b2 + hstep, voffB); PG8_STAGE(PG8_SA(0, 0), a2, voffA);
;             PG8_WAIT_V(8); PG8_WAIT_L(0); PG8_BAR; if (cur.half == 0) { PG8_MMA(1, 0, At, B0); PG8_MMA(1, 1, At, B1); } PG8_BAR; PG8_SCHED;
;             PG8_LDB(B0, 1, 0); PG8_LDB(B1, 1, 1); PG8_SCHED; PG8_LDA(At, 1, 0); PG8_STAGE(PG8_SA(0, 1), a2 + hstep, voffA);
;             PG8_WAIT_V(8); PG8_WAIT_L(0); PG8_BAR; PG8_MMA(0, 0, At, B0); PG8_MMA(0, 1, At, B1); PG8_BAR; PG8_SCHED;
.LBB0_1477:
	s_add_u32 s0, s26, 0xfffc0080
	s_addc_u32 s1, s27, -1
	s_add_i32 s67, 0, 0x10000
	s_cmp_eq_u32 s66, 12
	s_cselect_b32 s29, s17, s1
	s_cselect_b32 s28, s62, s0
	v_add_u32_e32 v151, s67, v147
	s_cselect_b32 s1, s19, s65
	s_cselect_b32 s0, s63, s64
	s_add_i32 s70, 0, 0x14000
	ds_read_b128 v[142:145], v151
	ds_read_b128 v[152:155], v151 offset:1024
	ds_read_b128 v[156:159], v151 offset:2048
	ds_read_b128 v[160:163], v151 offset:3072
	v_add_u32_e32 v151, s70, v147
	ds_read_b128 v[164:167], v151
	ds_read_b128 v[168:171], v151 offset:1024
	ds_read_b128 v[172:175], v151 offset:2048
	ds_read_b128 v[176:179], v151 offset:3072
	v_lshl_add_u64 v[212:213], s[26:27], 0, v[138:139]
	s_add_i32 m0, s15, 0xc000
	ds_read_b128 v[180:183], v150
	ds_read_b128 v[184:187], v150 offset:1024
	ds_read_b128 v[188:191], v150 offset:2048
	ds_read_b128 v[192:195], v150 offset:3072
	ds_read_b128 v[196:199], v150 offset:4096
	ds_read_b128 v[200:203], v150 offset:5120
	ds_read_b128 v[204:207], v150 offset:6144
	ds_read_b128 v[208:211], v150 offset:7168
	global_load_lds_dwordx4 v[212:213], off
	v_lshl_add_u64 v[212:213], s[26:27], 0, v[140:141]
	s_add_i32 m0, s15, 0xe000
	s_nop 0
	global_load_lds_dwordx4 v[212:213], off
	s_waitcnt vmcnt(8)
	s_waitcnt lgkmcnt(0)
	s_barrier
	s_setprio 1
	s_waitcnt lgkmcnt(0)
	v_mfma_f32_16x16x32_bf16 v[128:131], v[142:145], v[180:183], v[128:131]
	v_mfma_f32_16x16x32_bf16 v[124:127], v[156:159], v[180:183], v[124:127]
	v_mfma_f32_16x16x32_bf16 v[112:115], v[142:145], v[188:191], v[112:115]
	v_mfma_f32_16x16x32_bf16 v[108:111], v[156:159], v[188:191], v[108:111]
	v_mfma_f32_16x16x32_bf16 v[96:99], v[142:145], v[196:199], v[96:99]
	v_mfma_f32_16x16x32_bf16 v[92:95], v[156:159], v[196:199], v[92:95]
	v_mfma_f32_16x16x32_bf16 v[80:83], v[142:145], v[204:207], v[80:83]
	v_mfma_f32_16x16x32_bf16 v[76:79], v[156:159], v[204:207], v[76:79]
	v_mfma_f32_16x16x32_bf16 v[128:131], v[152:155], v[184:187], v[128:131]
	v_mfma_f32_16x16x32_bf16 v[124:127], v[160:163], v[184:187], v[124:127]
	v_mfma_f32_16x16x32_bf16 v[112:115], v[152:155], v[192:195], v[112:115]
	v_mfma_f32_16x16x32_bf16 v[108:111], v[160:163], v[192:195], v[108:111]
	v_mfma_f32_16x16x32_bf16 v[96:99], v[152:155], v[200:203], v[96:99]
	v_mfma_f32_16x16x32_bf16 v[92:95], v[160:163], v[200:203], v[92:95]
	v_mfma_f32_16x16x32_bf16 v[80:83], v[152:155], v[208:211], v[80:83]
	v_mfma_f32_16x16x32_bf16 v[76:79], v[160:163], v[208:211], v[76:79]
	s_setprio 0
	s_setprio 1
	v_mfma_f32_16x16x32_bf16 v[120:123], v[164:167], v[180:183], v[120:123]
	v_mfma_f32_16x16x32_bf16 v[116:119], v[172:175], v[180:183], v[116:119]
	v_mfma_f32_16x16x32_bf16 v[104:107], v[164:167], v[188:191], v[104:107]
	v_mfma_f32_16x16x32_bf16 v[100:103], v[172:175], v[188:191], v[100:103]
	v_mfma_f32_16x16x32_bf16 v[88:91], v[164:167], v[196:199], v[88:91]
	v_mfma_f32_16x16x32_bf16 v[84:87], v[172:175], v[196:199], v[84:87]
	v_mfma_f32_16x16x32_bf16 v[72:75], v[164:167], v[204:207], v[72:75]
	v_mfma_f32_16x16x32_bf16 v[68:71], v[172:175], v[204:207], v[68:71]
	v_mfma_f32_16x16x32_bf16 v[120:123], v[168:171], v[184:187], v[120:123]
	v_mfma_f32_16x16x32_bf16 v[116:119], v[176:179], v[184:187], v[116:119]
	v_mfma_f32_16x16x32_bf16 v[104:107], v[168:171], v[192:195], v[104:107]
	v_mfma_f32_16x16x32_bf16 v[100:103], v[176:179], v[192:195], v[100:103]
	v_mfma_f32_16x16x32_bf16 v[88:91], v[168:171], v[200:203], v[88:91]
	v_mfma_f32_16x16x32_bf16 v[84:87], v[176:179], v[200:203], v[84:87]
	v_mfma_f32_16x16x32_bf16 v[72:75], v[168:171], v[208:211], v[72:75]
	v_mfma_f32_16x16x32_bf16 v[68:71], v[176:179], v[208:211], v[68:71]
	s_setprio 0
	s_barrier
	s_add_i32 s67, s67, s25
	v_lshl_add_u64 v[212:213], s[0:1], 0, v[2:3]
	s_mov_b32 m0, s67
	ds_read_b128 v[180:183], v150 offset:16384
	ds_read_b128 v[184:187], v150 offset:17408
	ds_read_b128 v[188:191], v150 offset:18432
	ds_read_b128 v[192:195], v150 offset:19456
	ds_read_b128 v[196:199], v150 offset:20480
	ds_read_b128 v[200:203], v150 offset:21504
	ds_read_b128 v[204:207], v150 offset:22528
	ds_read_b128 v[208:211], v150 offset:23552
	global_load_lds_dwordx4 v[212:213], off
	s_add_i32 m0, s67, 0x2000
	s_add_u32 s68, s0, 0x40000
	v_lshl_add_u64 v[214:215], s[0:1], 0, v[136:137]
	s_addc_u32 s69, s1, 0
	s_add_i32 s67, s70, s25
	global_load_lds_dwordx4 v[214:215], off
	v_lshl_add_u64 v[216:217], s[68:69], 0, v[2:3]
	s_mov_b32 m0, s67
	v_lshl_add_u64 v[218:219], s[28:29], 0, v[134:135]
	global_load_lds_dwordx4 v[216:217], off
	v_lshl_add_u64 v[216:217], s[68:69], 0, v[136:137]
	s_add_i32 m0, s67, 0x2000
	s_nop 0
	global_load_lds_dwordx4 v[216:217], off
	v_lshl_add_u64 v[216:217], s[28:29], 0, v[132:133]
	s_mov_b32 m0, s15
	s_nop 0
	global_load_lds_dwordx4 v[216:217], off
	s_mov_b32 m0, s21
	s_nop 0
	global_load_lds_dwordx4 v[218:219], off
	s_nop 0
	s_waitcnt vmcnt(8)
	s_waitcnt lgkmcnt(0)
	s_barrier
; #define PG8_STAGE(bufoff, gbase, voff) do { _Pragma("unroll") for (int _i = 0; _i < 2; ++_i) \
;         __builtin_amdgcn_global_load_lds((const unsigned*)((const char*)(gbase) + (voff)[_i]), (PG8_LAS unsigned*)(lds + (bufoff) + ldsw + _i * 8192), 16, 0, 0); } while (0)
; #define PG8_LDA(dst, b, h) do { _Pragma("unroll") for (int m = 0; m < 4; ++m) _Pragma("unroll") for (int k = 0; k < 2; ++k) dst[m][k] = *(const PG8_LAS bf16x8*)(lds + PG8_SA(b, h) + aoff + m * 2048 + k * 1024); } while (0)
; #define PG8_LDB(dst, b, h) do { _Pragma("unroll") for (int n = 0; n < 2; ++n) _Pragma("unroll") for (int k = 0; k < 2; ++k) dst[n][k] = *(const PG8_LAS bf16x8*)(lds + PG8_SB(b, h) + boff + n * 2048 + k * 1024); } while (0)
; #define PG8_MMA(ai, bj, At, Bt) do { __builtin_amdgcn_s_setprio(1); _Pragma("unroll") for (int m = 0; m < 4; ++m) _Pragma("unroll") for (int n = 0; n < 2; ++n) _Pragma("unroll") for (int k = 0; k < 2; ++k) \
;         acc[ai][bj][m][n] = __builtin_amdgcn_mfma_f32_16x16x32_bf16(Bt[n][k], At[m][k], acc[ai][bj][m][n], 0, 0, 0); __builtin_amdgcn_s_setprio(0); } while (0)
; #define PG8_WAIT_V(n) asm volatile("s_waitcnt vmcnt(" #n ")" ::: "memory")
; #define PG8_WAIT_L(n) asm volatile("s_waitcnt lgkmcnt(" #n ")" ::: "memory")
; #define PG8_BAR __builtin_amdgcn_s_barrier()
; #define PG8_SCHED __builtin_amdgcn_sched_barrier(0)
; template <class Epi, class Sched, bool ALIGN_EPI = false, bool SP2 = false>
; __device__ __forceinline__ void gemm_phase(PG8_LAS unsigned char* lds, const Gemm g, const Sched& S, const Epi& E) {
;     ...
;             PG8_WAIT_V(8); PG8_WAIT_L(0); PG8_BAR; if (cur.half == 0) { PG8_MMA(1, 0, At, B0); PG8_MMA(1, 1, At, B1); } PG8_BAR; PG8_SCHED;
;             PG8_LDB(B0, 1, 0); PG8_LDB(B1, 1, 1); PG8_SCHED; PG8_LDA(At, 1, 0); PG8_STAGE(PG8_SA(0, 1), a2 + hstep, voffA);
;             PG8_WAIT_V(8); PG8_WAIT_L(0); PG8_BAR; PG8_MMA(0, 0, At, B0); PG8_MMA(0, 1, At, B1); PG8_BAR; PG8_SCHED;
;             PG8_LDA(At, 1, 1); PG8_STAGE(PG8_SB(1, 0), b3, voffB); PG8_STAGE(PG8_SB(1, 1), b3 + hstep, voffB); PG8_STAGE(PG8_SA(1, 0), a3, voffA);
;             PG8_WAIT_V(8); PG8_WAIT_L(0); PG8_BAR; if (cur.half == 0) { PG8_MMA(1, 0, At, B0); PG8_MMA(1, 1, At, B1); } PG8_BAR; PG8_SCHED;
	s_setprio 1
	s_waitcnt lgkmcnt(0)
	v_mfma_f32_16x16x32_bf16 v[64:67], v[142:145], v[180:183], v[64:67]
	v_mfma_f32_16x16x32_bf16 v[60:63], v[156:159], v[180:183], v[60:63]
	v_mfma_f32_16x16x32_bf16 v[48:51], v[142:145], v[188:191], v[48:51]
	v_mfma_f32_16x16x32_bf16 v[44:47], v[156:159], v[188:191], v[44:47]
	v_mfma_f32_16x16x32_bf16 v[32:35], v[142:145], v[196:199], v[32:35]
	v_mfma_f32_16x16x32_bf16 v[28:31], v[156:159], v[196:199], v[28:31]
	v_mfma_f32_16x16x32_bf16 v[16:19], v[142:145], v[204:207], v[16:19]
	v_mfma_f32_16x16x32_bf16 v[12:15], v[156:159], v[204:207], v[12:15]
	v_mfma_f32_16x16x32_bf16 v[64:67], v[152:155], v[184:187], v[64:67]
	v_mfma_f32_16x16x32_bf16 v[60:63], v[160:163], v[184:187], v[60:63]
	v_mfma_f32_16x16x32_bf16 v[48:51], v[152:155], v[192:195], v[48:51]
	v_mfma_f32_16x16x32_bf16 v[44:47], v[160:163], v[192:195], v[44:47]
	v_mfma_f32_16x16x32_bf16 v[32:35], v[152:155], v[200:203], v[32:35]
	v_mfma_f32_16x16x32_bf16 v[28:31], v[160:163], v[200:203], v[28:31]
	v_mfma_f32_16x16x32_bf16 v[16:19], v[152:155], v[208:211], v[16:19]
	v_mfma_f32_16x16x32_bf16 v[12:15], v[160:163], v[208:211], v[12:15]
	s_setprio 0
	s_setprio 1
	v_mfma_f32_16x16x32_bf16 v[56:59], v[164:167], v[180:183], v[56:59]
	v_mfma_f32_16x16x32_bf16 v[52:55], v[172:175], v[180:183], v[52:55]
	v_mfma_f32_16x16x32_bf16 v[40:43], v[164:167], v[188:191], v[40:43]
	v_mfma_f32_16x16x32_bf16 v[36:39], v[172:175], v[188:191], v[36:39]
	v_mfma_f32_16x16x32_bf16 v[24:27], v[164:167], v[196:199], v[24:27]
	v_mfma_f32_16x16x32_bf16 v[20:23], v[172:175], v[196:199], v[20:23]
	v_mfma_f32_16x16x32_bf16 v[8:11], v[164:167], v[204:207], v[8:11]
	v_mfma_f32_16x16x32_bf16 v[4:7], v[172:175], v[204:207], v[4:7]
	v_mfma_f32_16x16x32_bf16 v[56:59], v[168:171], v[184:187], v[56:59]
	v_mfma_f32_16x16x32_bf16 v[52:55], v[176:179], v[184:187], v[52:55]
	v_mfma_f32_16x16x32_bf16 v[40:43], v[168:171], v[192:195], v[40:43]
	v_mfma_f32_16x16x32_bf16 v[36:39], v[176:179], v[192:195], v[36:39]
	v_mfma_f32_16x16x32_bf16 v[24:27], v[168:171], v[200:203], v[24:27]
	v_mfma_f32_16x16x32_bf16 v[20:23], v[176:179], v[200:203], v[20:23]
	v_mfma_f32_16x16x32_bf16 v[8:11], v[168:171], v[208:211], v[8:11]
	v_mfma_f32_16x16x32_bf16 v[4:7], v[176:179], v[208:211], v[4:7]
	s_setprio 0
	s_barrier
	s_add_i32 s67, 0, 0x18000
	v_add_u32_e32 v151, s67, v147
	s_add_i32 s68, 0, 0x1c000
	ds_read_b128 v[142:145], v151
	ds_read_b128 v[152:155], v151 offset:1024
	ds_read_b128 v[156:159], v151 offset:2048
	ds_read_b128 v[160:163], v151 offset:3072
	v_add_u32_e32 v151, s68, v147
	ds_read_b128 v[164:167], v151
	ds_read_b128 v[168:171], v151 offset:1024
	ds_read_b128 v[172:175], v151 offset:2048
	ds_read_b128 v[176:179], v151 offset:3072
	s_add_u32 s28, s28, 0x40000
	s_addc_u32 s29, s29, 0
	s_mov_b32 m0, s36
	v_lshl_add_u64 v[220:221], s[28:29], 0, v[132:133]
	ds_read_b128 v[180:183], v150 offset:32768
	ds_read_b128 v[184:187], v150 offset:33792
	ds_read_b128 v[188:191], v150 offset:34816
	ds_read_b128 v[192:195], v150 offset:35840
	ds_read_b128 v[196:199], v150 offset:36864
	ds_read_b128 v[200:203], v150 offset:37888
	ds_read_b128 v[204:207], v150 offset:38912
	ds_read_b128 v[208:211], v150 offset:39936
	global_load_lds_dwordx4 v[220:221], off
	v_lshl_add_u64 v[220:221], s[28:29], 0, v[134:135]
	s_mov_b32 m0, s40
	s_nop 0
	global_load_lds_dwordx4 v[220:221], off
	s_nop 0
	s_waitcnt vmcnt(8)
	s_waitcnt lgkmcnt(0)
	s_barrier
	s_setprio 1
	s_waitcnt lgkmcnt(0)
	v_mfma_f32_16x16x32_bf16 v[128:131], v[142:145], v[180:183], v[128:131]
	v_mfma_f32_16x16x32_bf16 v[124:127], v[156:159], v[180:183], v[124:127]
	v_mfma_f32_16x16x32_bf16 v[112:115], v[142:145], v[188:191], v[112:115]
	v_mfma_f32_16x16x32_bf16 v[108:111], v[156:159], v[188:191], v[108:111]
	v_mfma_f32_16x16x32_bf16 v[96:99], v[142:145], v[196:199], v[96:99]
	v_mfma_f32_16x16x32_bf16 v[92:95], v[156:159], v[196:199], v[92:95]
	v_mfma_f32_16x16x32_bf16 v[80:83], v[142:145], v[204:207], v[80:83]
	v_mfma_f32_16x16x32_bf16 v[76:79], v[156:159], v[204:207], v[76:79]
	v_mfma_f32_16x16x32_bf16 v[128:131], v[152:155], v[184:187], v[128:131]
	v_mfma_f32_16x16x32_bf16 v[124:127], v[160:163], v[184:187], v[124:127]
	v_mfma_f32_16x16x32_bf16 v[112:115], v[152:155], v[192:195], v[112:115]
	v_mfma_f32_16x16x32_bf16 v[108:111], v[160:163], v[192:195], v[108:111]
	v_mfma_f32_16x16x32_bf16 v[96:99], v[152:155], v[200:203], v[96:99]
	v_mfma_f32_16x16x32_bf16 v[92:95], v[160:163], v[200:203], v[92:95]
	v_mfma_f32_16x16x32_bf16 v[80:83], v[152:155], v[208:211], v[80:83]
	v_mfma_f32_16x16x32_bf16 v[76:79], v[160:163], v[208:211], v[76:79]
	s_setprio 0
	s_setprio 1
	v_mfma_f32_16x16x32_bf16 v[120:123], v[164:167], v[180:183], v[120:123]
	v_mfma_f32_16x16x32_bf16 v[116:119], v[172:175], v[180:183], v[116:119]
	v_mfma_f32_16x16x32_bf16 v[104:107], v[164:167], v[188:191], v[104:107]
	v_mfma_f32_16x16x32_bf16 v[100:103], v[172:175], v[188:191], v[100:103]
	v_mfma_f32_16x16x32_bf16 v[88:91], v[164:167], v[196:199], v[88:91]
	v_mfma_f32_16x16x32_bf16 v[84:87], v[172:175], v[196:199], v[84:87]
	v_mfma_f32_16x16x32_bf16 v[72:75], v[164:167], v[204:207], v[72:75]
	v_mfma_f32_16x16x32_bf16 v[68:71], v[172:175], v[204:207], v[68:71]
	v_mfma_f32_16x16x32_bf16 v[120:123], v[168:171], v[184:187], v[120:123]
	v_mfma_f32_16x16x32_bf16 v[116:119], v[176:179], v[184:187], v[116:119]
	v_mfma_f32_16x16x32_bf16 v[104:107], v[168:171], v[192:195], v[104:107]
	v_mfma_f32_16x16x32_bf16 v[100:103], v[176:179], v[192:195], v[100:103]
	v_mfma_f32_16x16x32_bf16 v[88:91], v[168:171], v[200:203], v[88:91]
	v_mfma_f32_16x16x32_bf16 v[84:87], v[176:179], v[200:203], v[84:87]
	v_mfma_f32_16x16x32_bf16 v[72:75], v[168:171], v[208:211], v[72:75]
	v_mfma_f32_16x16x32_bf16 v[68:71], v[176:179], v[208:211], v[68:71]
	s_setprio 0
	s_barrier
; #define PG8_STAGE(bufoff, gbase, voff) do { _Pragma("unroll") for (int _i = 0; _i < 2; ++_i) \
;         __builtin_amdgcn_global_load_lds((const unsigned*)((const char*)(gbase) + (voff)[_i]), (PG8_LAS unsigned*)(lds + (bufoff) + ldsw + _i * 8192), 16, 0, 0); } while (0)
; #define PG8_LDA(dst, b, h) do { _Pragma("unroll") for (int m = 0; m < 4; ++m) _Pragma("unroll") for (int k = 0; k < 2; ++k) dst[m][k] = *(const PG8_LAS bf16x8*)(lds + PG8_SA(b, h) + aoff + m * 2048 + k * 1024); } while (0)
; #define PG8_MMA(ai, bj, At, Bt) do { __builtin_amdgcn_s_setprio(1); _Pragma("unroll") for (int m = 0; m < 4; ++m) _Pragma("unroll") for (int n = 0; n < 2; ++n) _Pragma("unroll") for (int k = 0; k < 2; ++k) \
;         acc[ai][bj][m][n] = __builtin_amdgcn_mfma_f32_16x16x32_bf16(Bt[n][k], At[m][k], acc[ai][bj][m][n], 0, 0, 0); __builtin_amdgcn_s_setprio(0); } while (0)
; #define PG8_WAIT_V(n) asm volatile("s_waitcnt vmcnt(" #n ")" ::: "memory")
; #define PG8_WAIT_L(n) asm volatile("s_waitcnt lgkmcnt(" #n ")" ::: "memory")
; #define PG8_BAR __builtin_amdgcn_s_barrier()
; #define PG8_SCHED __builtin_amdgcn_sched_barrier(0)
; template <class Epi, class Sched, bool ALIGN_EPI = false, bool SP2 = false>
; __device__ __forceinline__ void gemm_phase(PG8_LAS unsigned char* lds, const Gemm g, const Sched& S, const Epi& E) {
;     ...
;             PG8_LDA(At, 1, 1); PG8_STAGE(PG8_SB(1, 0), b3, voffB); PG8_STAGE(PG8_SB(1, 1), b3 + hstep, voffB); PG8_STAGE(PG8_SA(1, 0), a3, voffA);
;             PG8_WAIT_V(8); PG8_WAIT_L(0); PG8_BAR; if (cur.half == 0) { PG8_MMA(1, 0, At, B0); PG8_MMA(1, 1, At, B1); } PG8_BAR; PG8_SCHED;
	s_add_i32 s28, s67, s25
	v_lshl_add_u64 v[212:213], v[212:213], 0, s[42:43]
	s_mov_b32 m0, s28
	ds_read_b128 v[180:183], v150 offset:49152
	ds_read_b128 v[184:187], v150 offset:50176
	ds_read_b128 v[188:191], v150 offset:51200
	ds_read_b128 v[192:195], v150 offset:52224
	ds_read_b128 v[196:199], v150 offset:53248
	ds_read_b128 v[200:203], v150 offset:54272
	ds_read_b128 v[204:207], v150 offset:55296
	ds_read_b128 v[208:211], v150 offset:56320
	global_load_lds_dwordx4 v[212:213], off
	s_add_i32 m0, s28, 0x2000
	s_add_u32 s0, s0, 0x40080
	v_lshl_add_u64 v[212:213], v[214:215], 0, s[42:43]
	s_addc_u32 s1, s1, 0
	s_add_i32 s28, s68, s25
	global_load_lds_dwordx4 v[212:213], off
	v_lshl_add_u64 v[212:213], s[0:1], 0, v[2:3]
	s_mov_b32 m0, s28
	s_nop 0
	global_load_lds_dwordx4 v[212:213], off
	v_lshl_add_u64 v[212:213], s[0:1], 0, v[136:137]
	s_add_i32 m0, s28, 0x2000
	s_nop 0
	global_load_lds_dwordx4 v[212:213], off
	v_lshl_add_u64 v[212:213], v[216:217], 0, s[42:43]
	s_mov_b32 m0, s41
	s_nop 0
	global_load_lds_dwordx4 v[212:213], off
	v_lshl_add_u64 v[212:213], v[218:219], 0, s[42:43]
	s_mov_b32 m0, s60
	s_nop 0
	global_load_lds_dwordx4 v[212:213], off
	s_waitcnt vmcnt(8)
	s_waitcnt lgkmcnt(0)
	s_barrier
	s_setprio 1
	s_waitcnt lgkmcnt(0)
	v_mfma_f32_16x16x32_bf16 v[64:67], v[142:145], v[180:183], v[64:67]
	v_mfma_f32_16x16x32_bf16 v[60:63], v[156:159], v[180:183], v[60:63]
	v_mfma_f32_16x16x32_bf16 v[48:51], v[142:145], v[188:191], v[48:51]
	v_mfma_f32_16x16x32_bf16 v[44:47], v[156:159], v[188:191], v[44:47]
	v_mfma_f32_16x16x32_bf16 v[32:35], v[142:145], v[196:199], v[32:35]
	v_mfma_f32_16x16x32_bf16 v[28:31], v[156:159], v[196:199], v[28:31]
	v_mfma_f32_16x16x32_bf16 v[16:19], v[142:145], v[204:207], v[16:19]
	v_mfma_f32_16x16x32_bf16 v[12:15], v[156:159], v[204:207], v[12:15]
	v_mfma_f32_16x16x32_bf16 v[64:67], v[152:155], v[184:187], v[64:67]
	v_mfma_f32_16x16x32_bf16 v[60:63], v[160:163], v[184:187], v[60:63]
	v_mfma_f32_16x16x32_bf16 v[48:51], v[152:155], v[192:195], v[48:51]
	v_mfma_f32_16x16x32_bf16 v[44:47], v[160:163], v[192:195], v[44:47]
	v_mfma_f32_16x16x32_bf16 v[32:35], v[152:155], v[200:203], v[32:35]
	v_mfma_f32_16x16x32_bf16 v[28:31], v[160:163], v[200:203], v[28:31]
	v_mfma_f32_16x16x32_bf16 v[16:19], v[152:155], v[208:211], v[16:19]
	v_mfma_f32_16x16x32_bf16 v[12:15], v[160:163], v[208:211], v[12:15]
	s_setprio 0
	s_setprio 1
	v_mfma_f32_16x16x32_bf16 v[56:59], v[164:167], v[180:183], v[56:59]
	v_mfma_f32_16x16x32_bf16 v[52:55], v[172:175], v[180:183], v[52:55]
	v_mfma_f32_16x16x32_bf16 v[40:43], v[164:167], v[188:191], v[40:43]
	v_mfma_f32_16x16x32_bf16 v[36:39], v[172:175], v[188:191], v[36:39]
	v_mfma_f32_16x16x32_bf16 v[24:27], v[164:167], v[196:199], v[24:27]
	v_mfma_f32_16x16x32_bf16 v[20:23], v[172:175], v[196:199], v[20:23]
	v_mfma_f32_16x16x32_bf16 v[8:11], v[164:167], v[204:207], v[8:11]
	v_mfma_f32_16x16x32_bf16 v[4:7], v[172:175], v[204:207], v[4:7]
	v_mfma_f32_16x16x32_bf16 v[56:59], v[168:171], v[184:187], v[56:59]
	v_mfma_f32_16x16x32_bf16 v[52:55], v[176:179], v[184:187], v[52:55]
	v_mfma_f32_16x16x32_bf16 v[40:43], v[168:171], v[192:195], v[40:43]
	v_mfma_f32_16x16x32_bf16 v[36:39], v[176:179], v[192:195], v[36:39]
	v_mfma_f32_16x16x32_bf16 v[24:27], v[168:171], v[200:203], v[24:27]
	v_mfma_f32_16x16x32_bf16 v[20:23], v[176:179], v[200:203], v[20:23]
	v_mfma_f32_16x16x32_bf16 v[8:11], v[168:171], v[208:211], v[8:11]
	v_mfma_f32_16x16x32_bf16 v[4:7], v[176:179], v[208:211], v[4:7]
	s_setprio 0
	s_barrier
	s_add_i32 s66, s66, 2
	s_add_u32 s26, s26, 0x100
	s_addc_u32 s27, s27, 0
	s_add_u32 s64, s64, 0x100
	s_addc_u32 s65, s65, 0
	s_cmp_gt_u32 s66, 13
	s_cbranch_scc0 .LBB0_1477
	s_and_b64 vcc, exec, s[12:13]
	s_cbranch_vccz .LBB0_1480
	s_barrier

; __device__ __forceinline__ unsigned xb_ld(unsigned* p)              { return __hip_atomic_load(p, __ATOMIC_RELAXED, __HIP_MEMORY_SCOPE_AGENT); }
; __device__ __forceinline__ unsigned xb_add(unsigned* p, unsigned v) { return __hip_atomic_fetch_add(p, v, __ATOMIC_RELAXED, __HIP_MEMORY_SCOPE_AGENT); }
; #define XB_SPIN(cond, bar) do { unsigned _sp = 0; while (cond) { __builtin_amdgcn_s_sleep(1); \
;     if ((++_sp & 255u) == 0u) { if (xb_ld(&(bar)[XB_TMO])) break; if (_sp > XB_SPIN_CAP) { atomicAdd(&(bar)[XB_TMO], 1u); break; } } } } while (0)
; __device__ __forceinline__ void xcd_barrier(const XcdBarrier& b, const bool group_local = false, const bool xcc_only = false) {
;     ...
;         if (old + 1u == (gen + 1u) * nloc) {
;             const bool fast = group_local && b.st[2] == 2u;
;             if (!fast) {
;             __builtin_amdgcn_fence(__ATOMIC_RELEASE, "agent");
;             asm volatile("s_waitcnt vmcnt(0)" ::: "memory"); }
;             if (!(fast && xcc_only)) {
;             const unsigned og = xb_add(&bar[XB_TOP], 1u);
;             const unsigned tg = og / nx;
;             if (og + 1u == (tg + 1u) * nx) xb_add(&bar[XB_TOPGEN], 1u);
;             else XB_SPIN(xb_ld(&bar[XB_TOPGEN]) == tg, bar);
;             }
;             asm volatile("" ::: "memory");
;             xb_add(&bar[XB_XGEN(b.x)], 1u);
;             __builtin_amdgcn_fence(__ATOMIC_ACQUIRE, "agent");
;             asm volatile("s_waitcnt vmcnt(0)" ::: "memory");
;         } else {
;             XB_SPIN(xb_ld(&bar[XB_XGEN(b.x)]) <= gen, bar);
;     ...
;             __builtin_amdgcn_fence(__ATOMIC_ACQUIRE, "agent");
;     ...
;             asm volatile("s_waitcnt vmcnt(0)" ::: "memory");
;         }
.LBB0_1729:
	s_add_u32 s4, s6, 0x2400
	s_addc_u32 s5, s7, 0
	v_mov_b64_e32 v[4:5], s[4:5]
	s_or_b64 s[12:13], s[12:13], exec
	s_or_b64 exec, exec, s[0:1]
	s_and_saveexec_b64 s[0:1], s[12:13]
	s_cbranch_execnz .LBB0_1427
	s_branch .LBB0_1428
	.p2align 6
	s_nop 0
	s_nop 0
	s_nop 0
.LBB0_1730:
	s_or_b64 exec, exec, s[26:27]
	s_and_b64 s[26:27], s[28:29], exec

;     __device__ __forceinline__ void a_ready(const Unit&) const { if (++ncall == 3 && sig != nullptr && threadIdx.x == 0) __hip_atomic_fetch_add(sig, 1u, __ATOMIC_RELAXED, __HIP_MEMORY_SCOPE_AGENT); }
; #define PG8_STAGE(bufoff, gbase, voff) do { _Pragma("unroll") for (int _i = 0; _i < 2; ++_i) \
;         __builtin_amdgcn_global_load_lds((const unsigned*)((const char*)(gbase) + (voff)[_i]), (PG8_LAS unsigned*)(lds + (bufoff) + ldsw + _i * 8192), 16, 0, 0); } while (0)
; #define PG8_LDA(dst, b, h) do { _Pragma("unroll") for (int m = 0; m < 4; ++m) _Pragma("unroll") for (int k = 0; k < 2; ++k) dst[m][k] = *(const PG8_LAS bf16x8*)(lds + PG8_SA(b, h) + aoff + m * 2048 + k * 1024); } while (0)
; #define PG8_BAR __builtin_amdgcn_s_barrier()
; template <class Epi, class Sched, bool ALIGN_EPI = false, bool SP2 = false>
; __device__ __forceinline__ void gemm_phase(PG8_LAS unsigned char* lds, const Gemm g, const Sched& S, const Epi& E) {
;     ...
;         for (int t = 0; t < nt; t += 2) {
;             const bool last = (t == nt - 2);
;             const char* a1 = cA + (size_t)(t + 1) * kstep;
;             const char* a2 = last ? nA : cA + (size_t)(t + 2) * kstep; const char* b2 = last ? nB : cB + (size_t)(t + 2) * kstep;
;             const char* a3 = a2 + kstep; const char* b3 = b2 + kstep;
;             if (last && has_next) S.a_ready(nxt);
;             if constexpr (SP2) {
;             PG8_LDB(B0, 0, 0); PG8_LDB(B1, 0, 1); PG8_SCHED; PG8_LDA(At, 0, 0); PG8_STAGE(PG8_SA(1, 1), a1 + hstep, voffA);
;     ...
;             if (PROBE_KIND == 18 && t == 0 && ui > 0 && g.probe) { const unsigned long long tq_ = __builtin_amdgcn_s_memrealtime(); PG8_WAIT_V(8); pg8_probe_acc += (unsigned)(__builtin_amdgcn_s_memrealtime() - tq_); }
;     ...
;             PG8_WAIT_V(8); PG8_WAIT_L(0); PG8_BAR; PG8_MMA(0, 0, At, B0); PG8_MMA(0, 1, At, B1); PG8_BAR; PG8_SCHED;
;             PG8_LDA(At, 0, 1); PG8_STAGE(PG8_SB(0, 0), b2, voffB); PG8_STAGE(PG8_SB(0, 1), b2 + hstep, voffB); PG8_STAGE(PG8_SA(0, 0), a2, voffA);
;             PG8_WAIT_V(8); PG8_WAIT_L(0); PG8_BAR; if (cur.half == 0) { PG8_MMA(1, 0, At, B0); PG8_MMA(1, 1, At, B1); } PG8_BAR; PG8_SCHED;
;             PG8_LDB(B0, 1, 0); PG8_LDB(B1, 1, 1); PG8_SCHED; PG8_LDA(At, 1, 0); PG8_STAGE(PG8_SA(0, 1), a2 + hstep, voffA);
;             PG8_WAIT_V(8); PG8_WAIT_L(0); PG8_BAR; PG8_MMA(0, 0, At, B0); PG8_MMA(0, 1, At, B1); PG8_BAR; PG8_SCHED;
.LBB0_1780:
	s_add_u32 s18, s6, s0
	s_addc_u32 s19, s7, s1
	s_add_u32 s18, s18, 0x100
	s_addc_u32 s19, s19, 0
	s_add_u32 s63, s60, s0
	s_addc_u32 s64, s61, s1
	s_add_i32 s65, 0, 0x10000
	s_cmpk_eq_i32 s0, 0x1500
	s_cselect_b32 s21, s15, s19
	s_cselect_b32 s20, s14, s18
	s_cselect_b32 s19, s11, s64
	s_cselect_b32 s18, s10, s63
	s_add_i32 s63, 0, 0x14000
	v_add_u32_e32 v162, s65, v148
	v_add_u32_e32 v178, s63, v148
	ds_read_b128 v[150:153], v162
	ds_read_b128 v[154:157], v162 offset:1024
	ds_read_b128 v[158:161], v162 offset:2048
	ds_read_b128 v[162:165], v162 offset:3072
	ds_read_b128 v[166:169], v178
	ds_read_b128 v[170:173], v178 offset:1024
	ds_read_b128 v[174:177], v178 offset:2048
	ds_read_b128 v[178:181], v178 offset:3072
	v_lshl_add_u64 v[214:215], v[142:143], 0, s[0:1]
	s_add_i32 m0, s35, 0xc000
	ds_read_b128 v[182:185], v149
	ds_read_b128 v[186:189], v149 offset:1024
	ds_read_b128 v[190:193], v149 offset:2048
	ds_read_b128 v[194:197], v149 offset:3072
	ds_read_b128 v[198:201], v149 offset:4096
	ds_read_b128 v[202:205], v149 offset:5120
	ds_read_b128 v[206:209], v149 offset:6144
	ds_read_b128 v[210:213], v149 offset:7168
	global_load_lds_dwordx4 v[214:215], off
	v_lshl_add_u64 v[214:215], v[144:145], 0, s[0:1]
	s_add_i32 m0, s35, 0xe000
	s_nop 0
	global_load_lds_dwordx4 v[214:215], off
	s_waitcnt vmcnt(8)
	s_waitcnt lgkmcnt(0)
	s_barrier
	s_setprio 1
	s_waitcnt lgkmcnt(0)
	v_mfma_f32_16x16x32_bf16 v[128:131], v[150:153], v[182:185], v[128:131]
	v_mfma_f32_16x16x32_bf16 v[124:127], v[158:161], v[182:185], v[124:127]
	v_mfma_f32_16x16x32_bf16 v[112:115], v[150:153], v[190:193], v[112:115]
	v_mfma_f32_16x16x32_bf16 v[108:111], v[158:161], v[190:193], v[108:111]
	v_mfma_f32_16x16x32_bf16 v[96:99], v[150:153], v[198:201], v[96:99]
	v_mfma_f32_16x16x32_bf16 v[92:95], v[158:161], v[198:201], v[92:95]
	v_mfma_f32_16x16x32_bf16 v[80:83], v[150:153], v[206:209], v[80:83]
	v_mfma_f32_16x16x32_bf16 v[76:79], v[158:161], v[206:209], v[76:79]
	v_mfma_f32_16x16x32_bf16 v[128:131], v[154:157], v[186:189], v[128:131]
	v_mfma_f32_16x16x32_bf16 v[124:127], v[162:165], v[186:189], v[124:127]
	v_mfma_f32_16x16x32_bf16 v[112:115], v[154:157], v[194:197], v[112:115]
	v_mfma_f32_16x16x32_bf16 v[108:111], v[162:165], v[194:197], v[108:111]
	v_mfma_f32_16x16x32_bf16 v[96:99], v[154:157], v[202:205], v[96:99]
	v_mfma_f32_16x16x32_bf16 v[92:95], v[162:165], v[202:205], v[92:95]
	v_mfma_f32_16x16x32_bf16 v[80:83], v[154:157], v[210:213], v[80:83]
	v_mfma_f32_16x16x32_bf16 v[76:79], v[162:165], v[210:213], v[76:79]
	s_setprio 0
	s_setprio 1
	v_mfma_f32_16x16x32_bf16 v[120:123], v[166:169], v[182:185], v[120:123]
	v_mfma_f32_16x16x32_bf16 v[116:119], v[174:177], v[182:185], v[116:119]
	v_mfma_f32_16x16x32_bf16 v[104:107], v[166:169], v[190:193], v[104:107]
	v_mfma_f32_16x16x32_bf16 v[100:103], v[174:177], v[190:193], v[100:103]
	v_mfma_f32_16x16x32_bf16 v[88:91], v[166:169], v[198:201], v[88:91]
	v_mfma_f32_16x16x32_bf16 v[84:87], v[174:177], v[198:201], v[84:87]
	v_mfma_f32_16x16x32_bf16 v[72:75], v[166:169], v[206:209], v[72:75]
	v_mfma_f32_16x16x32_bf16 v[68:71], v[174:177], v[206:209], v[68:71]
	v_mfma_f32_16x16x32_bf16 v[120:123], v[170:173], v[186:189], v[120:123]
	v_mfma_f32_16x16x32_bf16 v[116:119], v[178:181], v[186:189], v[116:119]
	v_mfma_f32_16x16x32_bf16 v[104:107], v[170:173], v[194:197], v[104:107]
	v_mfma_f32_16x16x32_bf16 v[100:103], v[178:181], v[194:197], v[100:103]
	v_mfma_f32_16x16x32_bf16 v[88:91], v[170:173], v[202:205], v[88:91]
	v_mfma_f32_16x16x32_bf16 v[84:87], v[178:181], v[202:205], v[84:87]
	v_mfma_f32_16x16x32_bf16 v[72:75], v[170:173], v[210:213], v[72:75]
	v_mfma_f32_16x16x32_bf16 v[68:71], v[178:181], v[210:213], v[68:71]
	s_setprio 0
	s_barrier
	s_add_i32 s64, s65, s34
	v_lshl_add_u64 v[214:215], s[18:19], 0, v[2:3]
	s_mov_b32 m0, s64
	ds_read_b128 v[182:185], v149 offset:16384
	ds_read_b128 v[186:189], v149 offset:17408
	ds_read_b128 v[190:193], v149 offset:18432
	ds_read_b128 v[194:197], v149 offset:19456
	ds_read_b128 v[198:201], v149 offset:20480
	ds_read_b128 v[202:205], v149 offset:21504
	ds_read_b128 v[206:209], v149 offset:22528
	ds_read_b128 v[210:213], v149 offset:23552
	global_load_lds_dwordx4 v[214:215], off
	s_add_i32 m0, s64, 0x2000
	s_add_u32 s64, s18, 0xb0000
	v_lshl_add_u64 v[216:217], s[18:19], 0, v[136:137]
	s_addc_u32 s65, s19, 0
	s_add_i32 s63, s63, s34
	global_load_lds_dwordx4 v[216:217], off
	v_lshl_add_u64 v[218:219], s[64:65], 0, v[2:3]
	s_mov_b32 m0, s63
	v_lshl_add_u64 v[220:221], s[20:21], 0, v[134:135]
	global_load_lds_dwordx4 v[218:219], off
	v_lshl_add_u64 v[218:219], s[64:65], 0, v[136:137]
	s_add_i32 m0, s63, 0x2000
	s_nop 0
	global_load_lds_dwordx4 v[218:219], off
	v_lshl_add_u64 v[218:219], s[20:21], 0, v[132:133]
	s_mov_b32 m0, s35
	s_nop 0
	global_load_lds_dwordx4 v[218:219], off
	s_mov_b32 m0, s36
	s_nop 0
	global_load_lds_dwordx4 v[220:221], off
	s_nop 0
	s_waitcnt vmcnt(8)
	s_waitcnt lgkmcnt(0)
	s_barrier
; #define PG8_STAGE(bufoff, gbase, voff) do { _Pragma("unroll") for (int _i = 0; _i < 2; ++_i) \
;         __builtin_amdgcn_global_load_lds((const unsigned*)((const char*)(gbase) + (voff)[_i]), (PG8_LAS unsigned*)(lds + (bufoff) + ldsw + _i * 8192), 16, 0, 0); } while (0)
; #define PG8_LDA(dst, b, h) do { _Pragma("unroll") for (int m = 0; m < 4; ++m) _Pragma("unroll") for (int k = 0; k < 2; ++k) dst[m][k] = *(const PG8_LAS bf16x8*)(lds + PG8_SA(b, h) + aoff + m * 2048 + k * 1024); } while (0)
; #define PG8_LDB(dst, b, h) do { _Pragma("unroll") for (int n = 0; n < 2; ++n) _Pragma("unroll") for (int k = 0; k < 2; ++k) dst[n][k] = *(const PG8_LAS bf16x8*)(lds + PG8_SB(b, h) + boff + n * 2048 + k * 1024); } while (0)
; #define PG8_MMA(ai, bj, At, Bt) do { __builtin_amdgcn_s_setprio(1); _Pragma("unroll") for (int m = 0; m < 4; ++m) _Pragma("unroll") for (int n = 0; n < 2; ++n) _Pragma("unroll") for (int k = 0; k < 2; ++k) \
;         acc[ai][bj][m][n] = __builtin_amdgcn_mfma_f32_16x16x32_bf16(Bt[n][k], At[m][k], acc[ai][bj][m][n], 0, 0, 0); __builtin_amdgcn_s_setprio(0); } while (0)
; #define PG8_WAIT_V(n) asm volatile("s_waitcnt vmcnt(" #n ")" ::: "memory")
; #define PG8_WAIT_L(n) asm volatile("s_waitcnt lgkmcnt(" #n ")" ::: "memory")
; #define PG8_BAR __builtin_amdgcn_s_barrier()
; #define PG8_SCHED __builtin_amdgcn_sched_barrier(0)
; template <class Epi, class Sched, bool ALIGN_EPI = false, bool SP2 = false>
; __device__ __forceinline__ void gemm_phase(PG8_LAS unsigned char* lds, const Gemm g, const Sched& S, const Epi& E) {
;     ...
;             PG8_WAIT_V(8); PG8_WAIT_L(0); PG8_BAR; if (cur.half == 0) { PG8_MMA(1, 0, At, B0); PG8_MMA(1, 1, At, B1); } PG8_BAR; PG8_SCHED;
;             PG8_LDB(B0, 1, 0); PG8_LDB(B1, 1, 1); PG8_SCHED; PG8_LDA(At, 1, 0); PG8_STAGE(PG8_SA(0, 1), a2 + hstep, voffA);
;             PG8_WAIT_V(8); PG8_WAIT_L(0); PG8_BAR; PG8_MMA(0, 0, At, B0); PG8_MMA(0, 1, At, B1); PG8_BAR; PG8_SCHED;
;             PG8_LDA(At, 1, 1); PG8_STAGE(PG8_SB(1, 0), b3, voffB); PG8_STAGE(PG8_SB(1, 1), b3 + hstep, voffB); PG8_STAGE(PG8_SA(1, 0), a3, voffA);
;             PG8_WAIT_V(8); PG8_WAIT_L(0); PG8_BAR; if (cur.half == 0) { PG8_MMA(1, 0, At, B0); PG8_MMA(1, 1, At, B1); } PG8_BAR; PG8_SCHED;
	s_setprio 1
	s_waitcnt lgkmcnt(0)
	v_mfma_f32_16x16x32_bf16 v[64:67], v[150:153], v[182:185], v[64:67]
	v_mfma_f32_16x16x32_bf16 v[60:63], v[158:161], v[182:185], v[60:63]
	v_mfma_f32_16x16x32_bf16 v[48:51], v[150:153], v[190:193], v[48:51]
	v_mfma_f32_16x16x32_bf16 v[44:47], v[158:161], v[190:193], v[44:47]
	v_mfma_f32_16x16x32_bf16 v[32:35], v[150:153], v[198:201], v[32:35]
	v_mfma_f32_16x16x32_bf16 v[28:31], v[158:161], v[198:201], v[28:31]
	v_mfma_f32_16x16x32_bf16 v[16:19], v[150:153], v[206:209], v[16:19]
	v_mfma_f32_16x16x32_bf16 v[12:15], v[158:161], v[206:209], v[12:15]
	v_mfma_f32_16x16x32_bf16 v[64:67], v[154:157], v[186:189], v[64:67]
	v_mfma_f32_16x16x32_bf16 v[60:63], v[162:165], v[186:189], v[60:63]
	v_mfma_f32_16x16x32_bf16 v[48:51], v[154:157], v[194:197], v[48:51]
	v_mfma_f32_16x16x32_bf16 v[44:47], v[162:165], v[194:197], v[44:47]
	v_mfma_f32_16x16x32_bf16 v[32:35], v[154:157], v[202:205], v[32:35]
	v_mfma_f32_16x16x32_bf16 v[28:31], v[162:165], v[202:205], v[28:31]
	v_mfma_f32_16x16x32_bf16 v[16:19], v[154:157], v[210:213], v[16:19]
	v_mfma_f32_16x16x32_bf16 v[12:15], v[162:165], v[210:213], v[12:15]
	s_setprio 0
	s_setprio 1
	v_mfma_f32_16x16x32_bf16 v[56:59], v[166:169], v[182:185], v[56:59]
	v_mfma_f32_16x16x32_bf16 v[52:55], v[174:177], v[182:185], v[52:55]
	v_mfma_f32_16x16x32_bf16 v[40:43], v[166:169], v[190:193], v[40:43]
	v_mfma_f32_16x16x32_bf16 v[36:39], v[174:177], v[190:193], v[36:39]
	v_mfma_f32_16x16x32_bf16 v[24:27], v[166:169], v[198:201], v[24:27]
	v_mfma_f32_16x16x32_bf16 v[20:23], v[174:177], v[198:201], v[20:23]
	v_mfma_f32_16x16x32_bf16 v[8:11], v[166:169], v[206:209], v[8:11]
	v_mfma_f32_16x16x32_bf16 v[4:7], v[174:177], v[206:209], v[4:7]
	v_mfma_f32_16x16x32_bf16 v[56:59], v[170:173], v[186:189], v[56:59]
	v_mfma_f32_16x16x32_bf16 v[52:55], v[178:181], v[186:189], v[52:55]
	v_mfma_f32_16x16x32_bf16 v[40:43], v[170:173], v[194:197], v[40:43]
	v_mfma_f32_16x16x32_bf16 v[36:39], v[178:181], v[194:197], v[36:39]
	v_mfma_f32_16x16x32_bf16 v[24:27], v[170:173], v[202:205], v[24:27]
	v_mfma_f32_16x16x32_bf16 v[20:23], v[178:181], v[202:205], v[20:23]
	v_mfma_f32_16x16x32_bf16 v[8:11], v[170:173], v[210:213], v[8:11]
	v_mfma_f32_16x16x32_bf16 v[4:7], v[178:181], v[210:213], v[4:7]
	s_setprio 0
	s_barrier
	s_add_i32 s63, 0, 0x18000
	s_add_i32 s64, 0, 0x1c000
	v_add_u32_e32 v162, s63, v148
	v_add_u32_e32 v178, s64, v148
	ds_read_b128 v[150:153], v162
	ds_read_b128 v[154:157], v162 offset:1024
	ds_read_b128 v[158:161], v162 offset:2048
	ds_read_b128 v[162:165], v162 offset:3072
	ds_read_b128 v[166:169], v178
	ds_read_b128 v[170:173], v178 offset:1024
	ds_read_b128 v[174:177], v178 offset:2048
	ds_read_b128 v[178:181], v178 offset:3072
	s_add_u32 s20, s20, 0xb0000
	s_addc_u32 s21, s21, 0
	s_mov_b32 m0, s38
	v_lshl_add_u64 v[230:231], s[20:21], 0, v[132:133]
	ds_read_b128 v[182:185], v149 offset:32768
	ds_read_b128 v[186:189], v149 offset:33792
	ds_read_b128 v[190:193], v149 offset:34816
	ds_read_b128 v[194:197], v149 offset:35840
	ds_read_b128 v[198:201], v149 offset:36864
	ds_read_b128 v[202:205], v149 offset:37888
	ds_read_b128 v[206:209], v149 offset:38912
	ds_read_b128 v[210:213], v149 offset:39936
	global_load_lds_dwordx4 v[230:231], off
	v_lshl_add_u64 v[230:231], s[20:21], 0, v[134:135]
	s_mov_b32 m0, s39
	s_nop 0
	global_load_lds_dwordx4 v[230:231], off
	s_nop 0
	s_waitcnt vmcnt(8)
	s_waitcnt lgkmcnt(0)
	s_barrier
	s_setprio 1
	s_waitcnt lgkmcnt(0)
	v_mfma_f32_16x16x32_bf16 v[128:131], v[150:153], v[182:185], v[128:131]
	v_mfma_f32_16x16x32_bf16 v[124:127], v[158:161], v[182:185], v[124:127]
	v_mfma_f32_16x16x32_bf16 v[112:115], v[150:153], v[190:193], v[112:115]
	v_mfma_f32_16x16x32_bf16 v[108:111], v[158:161], v[190:193], v[108:111]
	v_mfma_f32_16x16x32_bf16 v[96:99], v[150:153], v[198:201], v[96:99]
	v_mfma_f32_16x16x32_bf16 v[92:95], v[158:161], v[198:201], v[92:95]
	v_mfma_f32_16x16x32_bf16 v[80:83], v[150:153], v[206:209], v[80:83]
	v_mfma_f32_16x16x32_bf16 v[76:79], v[158:161], v[206:209], v[76:79]
	v_mfma_f32_16x16x32_bf16 v[128:131], v[154:157], v[186:189], v[128:131]
	v_mfma_f32_16x16x32_bf16 v[124:127], v[162:165], v[186:189], v[124:127]
	v_mfma_f32_16x16x32_bf16 v[112:115], v[154:157], v[194:197], v[112:115]
	v_mfma_f32_16x16x32_bf16 v[108:111], v[162:165], v[194:197], v[108:111]
	v_mfma_f32_16x16x32_bf16 v[96:99], v[154:157], v[202:205], v[96:99]
	v_mfma_f32_16x16x32_bf16 v[92:95], v[162:165], v[202:205], v[92:95]
	v_mfma_f32_16x16x32_bf16 v[80:83], v[154:157], v[210:213], v[80:83]
	v_mfma_f32_16x16x32_bf16 v[76:79], v[162:165], v[210:213], v[76:79]
	s_setprio 0
	s_setprio 1
	v_mfma_f32_16x16x32_bf16 v[120:123], v[166:169], v[182:185], v[120:123]
	v_mfma_f32_16x16x32_bf16 v[116:119], v[174:177], v[182:185], v[116:119]
	v_mfma_f32_16x16x32_bf16 v[104:107], v[166:169], v[190:193], v[104:107]
	v_mfma_f32_16x16x32_bf16 v[100:103], v[174:177], v[190:193], v[100:103]
	v_mfma_f32_16x16x32_bf16 v[88:91], v[166:169], v[198:201], v[88:91]
	v_mfma_f32_16x16x32_bf16 v[84:87], v[174:177], v[198:201], v[84:87]
	v_mfma_f32_16x16x32_bf16 v[72:75], v[166:169], v[206:209], v[72:75]
	v_mfma_f32_16x16x32_bf16 v[68:71], v[174:177], v[206:209], v[68:71]
	v_mfma_f32_16x16x32_bf16 v[120:123], v[170:173], v[186:189], v[120:123]
	v_mfma_f32_16x16x32_bf16 v[116:119], v[178:181], v[186:189], v[116:119]
	v_mfma_f32_16x16x32_bf16 v[104:107], v[170:173], v[194:197], v[104:107]
	v_mfma_f32_16x16x32_bf16 v[100:103], v[178:181], v[194:197], v[100:103]
	v_mfma_f32_16x16x32_bf16 v[88:91], v[170:173], v[202:205], v[88:91]
	v_mfma_f32_16x16x32_bf16 v[84:87], v[178:181], v[202:205], v[84:87]
	v_mfma_f32_16x16x32_bf16 v[72:75], v[170:173], v[210:213], v[72:75]
	v_mfma_f32_16x16x32_bf16 v[68:71], v[178:181], v[210:213], v[68:71]
	s_setprio 0
	s_barrier
; template <class Epi, class Sched, bool ALIGN_EPI = false, bool SP2 = false>
; __device__ __forceinline__ void gemm_phase(PG8_LAS unsigned char* lds, const Gemm g, const Sched& S, const Epi& E) {
;     ...
;         if (!has_next) break;
;         if constexpr (!Epi::CHAIN) {
; #pragma unroll
;         for (int a = 0; a < 2; ++a)
; #pragma unroll
;             for (int b = 0; b < 2; ++b)
; #pragma unroll
;                 for (int m = 0; m < 4; ++m)
; #pragma unroll
;                     for (int n = 0; n < 2; ++n) acc[a][b][m][n] = (f32x4){0.f, 0.f, 0.f, 0.f};
;         }
;         cur = nxt; cA = nA; cB = nB; ++ui;
	s_add_i32 s20, s63, s34
	v_lshl_add_u64 v[214:215], v[214:215], 0, s[42:43]
	s_mov_b32 m0, s20
	ds_read_b128 v[182:185], v149 offset:49152
	ds_read_b128 v[186:189], v149 offset:50176
	ds_read_b128 v[190:193], v149 offset:51200
	ds_read_b128 v[194:197], v149 offset:52224
	ds_read_b128 v[198:201], v149 offset:53248
	ds_read_b128 v[202:205], v149 offset:54272
	ds_read_b128 v[206:209], v149 offset:55296
	ds_read_b128 v[210:213], v149 offset:56320
	global_load_lds_dwordx4 v[214:215], off
	s_add_i32 m0, s20, 0x2000
	s_add_u32 s18, s18, 0xb0080
	v_lshl_add_u64 v[214:215], v[216:217], 0, s[42:43]
	s_addc_u32 s19, s19, 0
	s_add_i32 s20, s64, s34
	global_load_lds_dwordx4 v[214:215], off
	v_lshl_add_u64 v[214:215], s[18:19], 0, v[2:3]
	s_mov_b32 m0, s20
	s_nop 0
	global_load_lds_dwordx4 v[214:215], off
	v_lshl_add_u64 v[214:215], s[18:19], 0, v[136:137]
	s_add_i32 m0, s20, 0x2000
	s_nop 0
	global_load_lds_dwordx4 v[214:215], off
	v_lshl_add_u64 v[214:215], v[218:219], 0, s[42:43]
	s_mov_b32 m0, s40
	s_nop 0
	global_load_lds_dwordx4 v[214:215], off
	v_lshl_add_u64 v[214:215], v[220:221], 0, s[42:43]
	s_mov_b32 m0, s41
	s_nop 0
	global_load_lds_dwordx4 v[214:215], off
	s_waitcnt vmcnt(8)
	s_waitcnt lgkmcnt(0)
	s_barrier
	s_setprio 1
	s_waitcnt lgkmcnt(0)
	v_mfma_f32_16x16x32_bf16 v[64:67], v[150:153], v[182:185], v[64:67]
	v_mfma_f32_16x16x32_bf16 v[60:63], v[158:161], v[182:185], v[60:63]
	v_mfma_f32_16x16x32_bf16 v[48:51], v[150:153], v[190:193], v[48:51]
	v_mfma_f32_16x16x32_bf16 v[44:47], v[158:161], v[190:193], v[44:47]
	v_mfma_f32_16x16x32_bf16 v[32:35], v[150:153], v[198:201], v[32:35]
	v_mfma_f32_16x16x32_bf16 v[28:31], v[158:161], v[198:201], v[28:31]
	v_mfma_f32_16x16x32_bf16 v[16:19], v[150:153], v[206:209], v[16:19]
	v_mfma_f32_16x16x32_bf16 v[12:15], v[158:161], v[206:209], v[12:15]
	v_mfma_f32_16x16x32_bf16 v[64:67], v[154:157], v[186:189], v[64:67]
	v_mfma_f32_16x16x32_bf16 v[60:63], v[162:165], v[186:189], v[60:63]
	v_mfma_f32_16x16x32_bf16 v[48:51], v[154:157], v[194:197], v[48:51]
	v_mfma_f32_16x16x32_bf16 v[44:47], v[162:165], v[194:197], v[44:47]
	v_mfma_f32_16x16x32_bf16 v[32:35], v[154:157], v[202:205], v[32:35]
	v_mfma_f32_16x16x32_bf16 v[28:31], v[162:165], v[202:205], v[28:31]
	v_mfma_f32_16x16x32_bf16 v[16:19], v[154:157], v[210:213], v[16:19]
	v_mfma_f32_16x16x32_bf16 v[12:15], v[162:165], v[210:213], v[12:15]
	s_setprio 0
	s_setprio 1
	v_mfma_f32_16x16x32_bf16 v[56:59], v[166:169], v[182:185], v[56:59]
	v_mfma_f32_16x16x32_bf16 v[52:55], v[174:177], v[182:185], v[52:55]
	v_mfma_f32_16x16x32_bf16 v[40:43], v[166:169], v[190:193], v[40:43]
	v_mfma_f32_16x16x32_bf16 v[36:39], v[174:177], v[190:193], v[36:39]
	v_mfma_f32_16x16x32_bf16 v[24:27], v[166:169], v[198:201], v[24:27]
	v_mfma_f32_16x16x32_bf16 v[20:23], v[174:177], v[198:201], v[20:23]
	v_mfma_f32_16x16x32_bf16 v[8:11], v[166:169], v[206:209], v[8:11]
	v_mfma_f32_16x16x32_bf16 v[4:7], v[174:177], v[206:209], v[4:7]
	v_mfma_f32_16x16x32_bf16 v[56:59], v[170:173], v[186:189], v[56:59]
	v_mfma_f32_16x16x32_bf16 v[52:55], v[178:181], v[186:189], v[52:55]
	v_mfma_f32_16x16x32_bf16 v[40:43], v[170:173], v[194:197], v[40:43]
	v_mfma_f32_16x16x32_bf16 v[36:39], v[178:181], v[194:197], v[36:39]
	v_mfma_f32_16x16x32_bf16 v[24:27], v[170:173], v[202:205], v[24:27]
	v_mfma_f32_16x16x32_bf16 v[20:23], v[178:181], v[202:205], v[20:23]
	v_mfma_f32_16x16x32_bf16 v[8:11], v[170:173], v[210:213], v[8:11]
	v_mfma_f32_16x16x32_bf16 v[4:7], v[178:181], v[210:213], v[4:7]
	s_setprio 0
	s_barrier
	s_add_i32 s62, s62, 2
	s_add_u32 s0, s0, 0x100
	s_addc_u32 s1, s1, 0
	s_cmp_gt_u32 s62, 41
	s_cbranch_scc0 .LBB0_1780
	s_add_u32 s0, s60, 0xffffff00
	s_addc_u32 s1, s61, -1
	s_and_b64 vcc, exec, s[4:5]
	s_cbranch_vccnz .LBB0_1783
	v_mov_b32_e32 v4, 0
	s_mov_b32 s16, s58
	s_mov_b32 s23, s57
	s_mov_b64 s[6:7], s[14:15]
	s_mov_b32 s56, s59
	v_mov_b32_e32 v5, v4
	v_mov_b32_e32 v6, v4
	v_mov_b32_e32 v7, v4
	v_mov_b32_e32 v8, v4
	v_mov_b32_e32 v9, v4
	v_mov_b32_e32 v10, v4
	v_mov_b32_e32 v11, v4
	v_mov_b32_e32 v20, v4
	v_mov_b32_e32 v21, v4
	v_mov_b32_e32 v22, v4
	v_mov_b32_e32 v23, v4
	v_mov_b32_e32 v24, v4
	v_mov_b32_e32 v25, v4
	v_mov_b32_e32 v26, v4
	v_mov_b32_e32 v27, v4
	v_mov_b32_e32 v36, v4
	v_mov_b32_e32 v37, v4
	v_mov_b32_e32 v38, v4
	v_mov_b32_e32 v39, v4
	v_mov_b32_e32 v40, v4
	v_mov_b32_e32 v41, v4
	v_mov_b32_e32 v42, v4
	v_mov_b32_e32 v43, v4
	v_mov_b32_e32 v52, v4
	v_mov_b32_e32 v53, v4
	v_mov_b32_e32 v54, v4
	v_mov_b32_e32 v55, v4
	v_mov_b32_e32 v56, v4
	v_mov_b32_e32 v57, v4
	v_mov_b32_e32 v58, v4
	v_mov_b32_e32 v59, v4
	v_mov_b32_e32 v12, v4
	v_mov_b32_e32 v13, v4
	v_mov_b32_e32 v14, v4
	v_mov_b32_e32 v15, v4
	v_mov_b32_e32 v16, v4
	v_mov_b32_e32 v17, v4
	v_mov_b32_e32 v18, v4
	v_mov_b32_e32 v19, v4
	v_mov_b32_e32 v28, v4
	v_mov_b32_e32 v29, v4
	v_mov_b32_e32 v30, v4
	v_mov_b32_e32 v31, v4
	v_mov_b32_e32 v32, v4
	v_mov_b32_e32 v33, v4
	v_mov_b32_e32 v34, v4
	v_mov_b32_e32 v35, v4
	v_mov_b32_e32 v44, v4
	v_mov_b32_e32 v45, v4
	v_mov_b32_e32 v46, v4
	v_mov_b32_e32 v47, v4
	v_mov_b32_e32 v48, v4
	v_mov_b32_e32 v49, v4
	v_mov_b32_e32 v50, v4
	v_mov_b32_e32 v51, v4
	v_mov_b32_e32 v60, v4
	v_mov_b32_e32 v61, v4
	v_mov_b32_e32 v62, v4
	v_mov_b32_e32 v63, v4
	v_mov_b32_e32 v64, v4
	v_mov_b32_e32 v65, v4
	v_mov_b32_e32 v66, v4
	v_mov_b32_e32 v67, v4
	v_mov_b32_e32 v68, v4
	v_mov_b32_e32 v69, v4
	v_mov_b32_e32 v70, v4
	v_mov_b32_e32 v71, v4
	v_mov_b32_e32 v72, v4
	v_mov_b32_e32 v73, v4
	v_mov_b32_e32 v74, v4
	v_mov_b32_e32 v75, v4
	v_mov_b32_e32 v84, v4
	v_mov_b32_e32 v85, v4
	v_mov_b32_e32 v86, v4
	v_mov_b32_e32 v87, v4
	v_mov_b32_e32 v88, v4
	v_mov_b32_e32 v89, v4
	v_mov_b32_e32 v90, v4
	v_mov_b32_e32 v91, v4
	v_mov_b32_e32 v100, v4
	v_mov_b32_e32 v101, v4
	v_mov_b32_e32 v102, v4
	v_mov_b32_e32 v103, v4
	v_mov_b32_e32 v104, v4
	v_mov_b32_e32 v105, v4
	v_mov_b32_e32 v106, v4
	v_mov_b32_e32 v107, v4
	v_mov_b32_e32 v116, v4
	v_mov_b32_e32 v117, v4
	v_mov_b32_e32 v118, v4
	v_mov_b32_e32 v119, v4
	v_mov_b32_e32 v120, v4
	v_mov_b32_e32 v121, v4
	v_mov_b32_e32 v122, v4
	v_mov_b32_e32 v123, v4
	v_mov_b32_e32 v76, v4
	v_mov_b32_e32 v77, v4
	v_mov_b32_e32 v78, v4
	v_mov_b32_e32 v79, v4
	v_mov_b32_e32 v80, v4
	v_mov_b32_e32 v81, v4
	v_mov_b32_e32 v82, v4
	v_mov_b32_e32 v83, v4
	v_mov_b32_e32 v92, v4
	v_mov_b32_e32 v93, v4
	v_mov_b32_e32 v94, v4
	v_mov_b32_e32 v95, v4
	v_mov_b32_e32 v96, v4
	v_mov_b32_e32 v97, v4
	v_mov_b32_e32 v98, v4
	v_mov_b32_e32 v99, v4
	v_mov_b32_e32 v108, v4
	v_mov_b32_e32 v109, v4
	v_mov_b32_e32 v110, v4
	v_mov_b32_e32 v111, v4
	v_mov_b32_e32 v112, v4
	v_mov_b32_e32 v113, v4
	v_mov_b32_e32 v114, v4
	v_mov_b32_e32 v115, v4
	v_mov_b32_e32 v124, v4
	v_mov_b32_e32 v125, v4
	v_mov_b32_e32 v126, v4
	v_mov_b32_e32 v127, v4
	v_mov_b32_e32 v128, v4
	v_mov_b32_e32 v129, v4
	v_mov_b32_e32 v130, v4
	v_mov_b32_e32 v131, v4
	s_andn2_b64 vcc, exec, s[8:9]
	s_cbranch_vccnz .LBB0_1784
	s_branch .LBB0_1785
